# P6: x16 activation scale folded into the E8M0 block scale of the up-projection MFMAs (exact), 32 packed multiplies per unit removed from the SwiGLU epilogue
# baseline (speedup 1.0000x reference)
; #define PG8_STAGE(bufoff, gbase, voff) do { _Pragma("unroll") for (int _i = 0; _i < 2; ++_i) { unsigned keep_; \
;         asm volatile("s_mov_b32 %0, m0\n\ts_mov_b32 m0, %3\n\ts_nop 0\n\tglobal_load_lds_dwordx4 %1, %2\n\ts_mov_b32 m0, %0" : "=&s"(keep_) : "v"((voff)[_i]), "s"((const char*)(gbase)), "s"(ldsb + (unsigned)((bufoff) + _i * 8192)) : "memory"); } } while (0)
; #define PG8_WAIT_V(n) asm volatile("s_waitcnt vmcnt(" #n ")" ::: "memory")
; #define PG8_BAR __builtin_amdgcn_s_barrier()
; template <class Epi, class Sched, bool ALIGN_EPI, bool FP8 = false>
; __device__ __forceinline__ void gemm_phase(PG8_LAS unsigned char* lds, const Gemm g, const Sched& S, const Epi& E, const int wid, const int lane) {
;     ...
;     const int sa_v = g.sa, sb_v = g.sb;
;     ...
;     const char* cA = GA ? (const char*)g.A : (const char*)g.A + (size_t)cur.pm * tstep; const char* cB = (const char*)g.Bt + (size_t)cur.pn * tstep;
;     PG8_STAGE(PG8_SB(0, 0), cB, voffB); PG8_STAGE(PG8_SB(0, 1), cB + hstep, voffB); PG8_STAGE(PG8_SA(0, 0), cA, vc0); PG8_STAGE(PG8_SA(0, 1), cA + hstepA, vc1);
;     if (wr == 1) PG8_BAR;
;     PG8_WAIT_V(2); PG8_BAR;
;     PG8_STAGE(PG8_SB(1, 0), cB + kstep, voffB); PG8_STAGE(PG8_SA(1, 0), cA + kstep, vc0); PG8_STAGE(PG8_SB(1, 1), cB + hstep + kstep, voffB);
;     PG8_WAIT_V(6); PG8_BAR;
.LBB0_713:
	v_and_b32_e32 v0, 15, v10
	s_add_i32 s5, 0, 0x21800
	v_lshl_or_b32 v203, s4, 6, v0
	v_ashrrev_i32_e32 v2, 6, v10
	s_lshl_b32 s4, s4, 13
	v_lshl_add_u32 v201, v197, 4, s5
	s_lshr_b32 s5, s9, 25
	v_lshl_add_u32 v4, v2, 10, s4
	s_lshl_b32 s4, s80, 5
	s_add_i32 s5, s8, s5
	s_and_b32 s9, s4, 0x60
	s_ashr_i32 s68, s5, 7
	s_lshr_b32 s4, s9, 3
	s_add_u32 s24, s56, 0x45c00000
	s_addc_u32 s25, s57, 0
	v_add_lshl_u32 v2, v2, s4, 10
	s_add_u32 s4, s56, 0x41c00080
	s_addc_u32 s5, s57, 0
	s_add_u32 s26, s34, 0x80
	s_waitcnt vmcnt(2)
	s_barrier
	s_addc_u32 s27, s35, 0
	s_add_i32 s69, s47, 0x18000
	s_mov_b32 m0, s69
	s_nop 0
	global_load_lds_dwordx4 v200, s[26:27]
	s_add_i32 s70, s47, 0x1a000
	s_add_i32 s71, s47, 0x8000
	s_add_i32 s72, s47, 0xa000
	s_mov_b32 m0, s70
	s_nop 0
	global_load_lds_dwordx4 v202, s[26:27]
	s_add_u32 s0, s0, 0x80
	s_mov_b32 m0, s71
	s_nop 0
	global_load_lds_dwordx4 v64, s[4:5]
	s_addc_u32 s1, s1, 0
	s_add_i32 s73, s47, 0x1c000
	s_add_i32 s74, s47, 0x1e000
	v_and_b32_e32 v3, 48, v10
	s_mov_b32 m0, s72
	s_nop 0
	global_load_lds_dwordx4 v65, s[4:5]
	s_cmpk_gt_i32 s8, 0x7f
	v_lshl_or_b32 v0, v0, 6, v3
	v_lshlrev_b32_e32 v3, 2, v10
	s_mov_b32 m0, s73
	s_nop 0
	global_load_lds_dwordx4 v200, s[0:1]
	s_cselect_b64 s[26:27], -1, 0
	s_add_i32 s75, s68, -2
	s_add_i32 s83, s47, 0xc000
	v_ashrrev_i32_e32 v1, 1, v10
	v_and_b32_e32 v3, 32, v3
	s_mov_b32 m0, s74
	s_nop 0
	global_load_lds_dwordx4 v202, s[0:1]
	s_cmpk_lt_u32 s90, 0x100
	v_and_b32_e32 v1, -8, v1
	v_bitop3_b32 v4, v0, v4, v3 bitop3:0xde
	v_bitop3_b32 v0, v0, v2, v3 bitop3:0xde
	s_waitcnt vmcnt(6)
	s_cselect_b64 s[28:29], -1, 0
	s_ashr_i32 s0, s76, 3
	v_add_u32_e32 v205, s9, v1
	s_mul_i32 s85, s0, s3
	v_cndmask_b32_e64 v1, 0, 1, s[6:7]
	v_add_u32_e32 v206, 0, v0
	s_add_i32 s84, s47, 0xe000
	s_add_i32 s85, s85, s44
	v_cmp_ne_u32_e64 s[0:1], 1, v1
	v_add_u32_e32 v207, 0x10000, v206
	v_add_u32_e32 v208, 0x14000, v206
	v_add_u32_e32 v209, 0, v4
	v_mov_b32_e32 v210, 0x79
	v_mov_b32_e32 v211, 0x7f
	v_mov_b32_e32 v212, 0x7d
	s_barrier
	s_branch .LBB0_716

; #define PG8_STAGE(bufoff, gbase, voff) do { _Pragma("unroll") for (int _i = 0; _i < 2; ++_i) { unsigned keep_; \
;         asm volatile("s_mov_b32 %0, m0\n\ts_mov_b32 m0, %3\n\ts_nop 0\n\tglobal_load_lds_dwordx4 %1, %2\n\ts_mov_b32 m0, %0" : "=&s"(keep_) : "v"((voff)[_i]), "s"((const char*)(gbase)), "s"(ldsb + (unsigned)((bufoff) + _i * 8192)) : "memory"); } } while (0)
; #define PG8_LDA(dst, b, h) do { _Pragma("unroll") for (int m = 0; m < 4; ++m) _Pragma("unroll") for (int k = 0; k < 2; ++k) dst[m][k] = *(const PG8_LAS bf16x8*)(lds + PG8_SA(b, h) + aoff + m * 2048 + k * 1024); } while (0)
; #define PG8_LDB(dst, b, h) do { _Pragma("unroll") for (int n = 0; n < 2; ++n) _Pragma("unroll") for (int k = 0; k < 2; ++k) dst[n][k] = *(const PG8_LAS bf16x8*)(lds + PG8_SB(b, h) + boff + n * 2048 + k * 1024); } while (0)
; #define PG8_WAIT_V(n) asm volatile("s_waitcnt vmcnt(" #n ")" ::: "memory")
; #define PG8_WAIT_L(n) asm volatile("s_waitcnt lgkmcnt(" #n ")" ::: "memory")
; #define PG8_BAR __builtin_amdgcn_s_barrier()
; #define PG8_SCHED __builtin_amdgcn_sched_barrier(0)
; template <class Epi, class Sched, bool ALIGN_EPI, bool FP8 = false>
; __device__ __forceinline__ void gemm_phase(PG8_LAS unsigned char* lds, const Gemm g, const Sched& S, const Epi& E, const int wid, const int lane) {
;     ...
;         for (int t = 0; t < nt; t += 2) {
;             const bool last = (t == nt - 2);
;             const char* a1 = cA + (size_t)(t + 1) * kstep;
;             const char* a2 = last ? nA : cA + (size_t)(t + 2) * kstep; const char* b2 = last ? nB : cB + (size_t)(t + 2) * kstep;
;             const char* a3 = a2 + kstep; const char* b3 = b2 + kstep;
;             PG8_LDB(B0, 0, 0); PG8_LDB(B1, 0, 1); PG8_SCHED; PG8_LDA(At, 0, 0); PG8_STAGE(PG8_SA(1, 1), a1 + hstepA, vc1);
;             if (GA && last && has_next) { const u32x4 q = *gslot; vc0[0] = q.x; vc0[1] = q.y; vc1[0] = q.z; vc1[1] = q.w; }
;             PG8_WAIT_V(8); PG8_WAIT_L(0); PG8_BAR; PG8_MMA(0, 0, At, B0); PG8_MMA(0, 1, At, B1); PG8_BAR; PG8_SCHED;
;             PG8_LDA(At, 0, 1); PG8_STAGE(PG8_SB(0, 0), b2, voffB); PG8_STAGE(PG8_SB(0, 1), b2 + hstep, voffB); PG8_STAGE(PG8_SA(0, 0), a2, vc0);
;             PG8_WAIT_V(8); PG8_WAIT_L(0); PG8_BAR; PG8_MMA(1, 0, At, B0); PG8_MMA(1, 1, At, B1); PG8_BAR; PG8_SCHED;
.LBB0_727:
	s_add_i32 s82, s82, 2
	s_and_b64 s[8:9], s[38:39], exec
	s_cselect_b32 s9, 0, s6
	s_cselect_b32 s8, 0, s7
	s_add_u32 s40, s20, s9
	s_addc_u32 s41, s21, s8
	s_add_u32 s33, s34, s6
	s_addc_u32 s42, s35, s7
	s_add_u32 s8, s40, 0x80
	s_addc_u32 s9, s41, 0
	s_waitcnt vmcnt(8)
	s_and_b64 s[38:39], s[38:39], exec
	s_waitcnt lgkmcnt(0)
	s_cselect_b32 s43, s31, s42
	s_cselect_b32 s42, s30, s33
	s_add_u32 s38, s42, 0x80
	s_addc_u32 s39, s43, 0
	s_barrier
	s_setprio 1
	s_waitcnt lgkmcnt(6)
	v_mfma_scale_f32_16x16x128_f8f6f4 v[192:195], v[24:31], v[56:63], v[192:195], v210, v211 op_sel_hi:[0,0,0]
	v_mfma_scale_f32_16x16x128_f8f6f4 v[184:187], v[16:23], v[56:63], v[184:187], v210, v211 op_sel_hi:[0,0,0]
	s_waitcnt lgkmcnt(4)
	v_mfma_scale_f32_16x16x128_f8f6f4 v[176:179], v[24:31], v[48:55], v[176:179], v210, v211 op_sel_hi:[0,0,0]
	v_mfma_scale_f32_16x16x128_f8f6f4 v[168:171], v[16:23], v[48:55], v[168:171], v210, v211 op_sel_hi:[0,0,0]
	s_waitcnt lgkmcnt(2)
	v_mfma_scale_f32_16x16x128_f8f6f4 v[160:163], v[24:31], v[40:47], v[160:163], v210, v211 op_sel_hi:[0,0,0]
	v_mfma_scale_f32_16x16x128_f8f6f4 v[152:155], v[16:23], v[40:47], v[152:155], v210, v211 op_sel_hi:[0,0,0]
	s_waitcnt lgkmcnt(0)
	v_mfma_scale_f32_16x16x128_f8f6f4 v[144:147], v[24:31], v[32:39], v[144:147], v210, v211 op_sel_hi:[0,0,0]
	v_mfma_scale_f32_16x16x128_f8f6f4 v[136:139], v[16:23], v[32:39], v[136:139], v210, v211 op_sel_hi:[0,0,0]
	s_setprio 0
	s_setprio 1
	v_mfma_scale_f32_16x16x128_f8f6f4 v[188:191], v[8:15], v[56:63], v[188:191], v212, v211 op_sel_hi:[0,0,0]
	v_mfma_scale_f32_16x16x128_f8f6f4 v[180:183], v[0:7], v[56:63], v[180:183], v212, v211 op_sel_hi:[0,0,0]
	v_mfma_scale_f32_16x16x128_f8f6f4 v[172:175], v[8:15], v[48:55], v[172:175], v212, v211 op_sel_hi:[0,0,0]
	v_mfma_scale_f32_16x16x128_f8f6f4 v[164:167], v[0:7], v[48:55], v[164:167], v212, v211 op_sel_hi:[0,0,0]
	v_mfma_scale_f32_16x16x128_f8f6f4 v[156:159], v[8:15], v[40:47], v[156:159], v212, v211 op_sel_hi:[0,0,0]
	v_mfma_scale_f32_16x16x128_f8f6f4 v[148:151], v[0:7], v[40:47], v[148:151], v212, v211 op_sel_hi:[0,0,0]
	v_mfma_scale_f32_16x16x128_f8f6f4 v[140:143], v[8:15], v[32:39], v[140:143], v212, v211 op_sel_hi:[0,0,0]
	v_mfma_scale_f32_16x16x128_f8f6f4 v[132:135], v[0:7], v[32:39], v[132:135], v212, v211 op_sel_hi:[0,0,0]
	s_setprio 0
	s_barrier
	ds_read_b128 v[32:35], v209 offset:16384
	ds_read_b128 v[36:39], v209 offset:17408
	ds_read_b128 v[40:43], v209 offset:18432
	ds_read_b128 v[44:47], v209 offset:19456
	ds_read_b128 v[48:51], v209 offset:20480
	ds_read_b128 v[52:55], v209 offset:21504
	ds_read_b128 v[56:59], v209 offset:22528
	ds_read_b128 v[60:63], v209 offset:23552
	s_mov_b32 m0, s51
	s_nop 0
	global_load_lds_dwordx4 v200, s[42:43]
	s_mov_b32 m0, s53
	s_nop 0
	global_load_lds_dwordx4 v202, s[42:43]
	s_add_u32 s42, s42, s16
	s_addc_u32 s43, s43, s17
	s_mov_b32 m0, s55
	s_nop 0
	global_load_lds_dwordx4 v200, s[42:43]
	s_mov_b32 m0, s64
	s_nop 0
	global_load_lds_dwordx4 v202, s[42:43]
	s_mov_b32 m0, s47
	s_nop 0
	global_load_lds_dwordx4 v64, s[40:41]
	s_mov_b32 m0, s65
	s_nop 0
	global_load_lds_dwordx4 v65, s[40:41]
	s_waitcnt vmcnt(8)
	s_waitcnt lgkmcnt(0)
	s_barrier
	s_setprio 1
	s_waitcnt lgkmcnt(6)
	v_mfma_scale_f32_16x16x128_f8f6f4 v[128:131], v[24:31], v[32:39], v[128:131], v210, v211 op_sel_hi:[0,0,0]
	v_mfma_scale_f32_16x16x128_f8f6f4 v[120:123], v[16:23], v[32:39], v[120:123], v210, v211 op_sel_hi:[0,0,0]
	s_waitcnt lgkmcnt(4)
	v_mfma_scale_f32_16x16x128_f8f6f4 v[112:115], v[24:31], v[40:47], v[112:115], v210, v211 op_sel_hi:[0,0,0]
	v_mfma_scale_f32_16x16x128_f8f6f4 v[104:107], v[16:23], v[40:47], v[104:107], v210, v211 op_sel_hi:[0,0,0]
	s_waitcnt lgkmcnt(2)
	v_mfma_scale_f32_16x16x128_f8f6f4 v[96:99], v[24:31], v[48:55], v[96:99], v210, v211 op_sel_hi:[0,0,0]
	v_mfma_scale_f32_16x16x128_f8f6f4 v[88:91], v[16:23], v[48:55], v[88:91], v210, v211 op_sel_hi:[0,0,0]
	s_waitcnt lgkmcnt(0)
	v_mfma_scale_f32_16x16x128_f8f6f4 v[80:83], v[24:31], v[56:63], v[80:83], v210, v211 op_sel_hi:[0,0,0]
	v_mfma_scale_f32_16x16x128_f8f6f4 v[72:75], v[16:23], v[56:63], v[72:75], v210, v211 op_sel_hi:[0,0,0]
	s_setprio 0
	s_setprio 1
	v_mfma_scale_f32_16x16x128_f8f6f4 v[124:127], v[8:15], v[32:39], v[124:127], v212, v211 op_sel_hi:[0,0,0]
	v_mfma_scale_f32_16x16x128_f8f6f4 v[116:119], v[0:7], v[32:39], v[116:119], v212, v211 op_sel_hi:[0,0,0]
	v_mfma_scale_f32_16x16x128_f8f6f4 v[108:111], v[8:15], v[40:47], v[108:111], v212, v211 op_sel_hi:[0,0,0]
	v_mfma_scale_f32_16x16x128_f8f6f4 v[100:103], v[0:7], v[40:47], v[100:103], v212, v211 op_sel_hi:[0,0,0]
	v_mfma_scale_f32_16x16x128_f8f6f4 v[92:95], v[8:15], v[48:55], v[92:95], v212, v211 op_sel_hi:[0,0,0]
	v_mfma_scale_f32_16x16x128_f8f6f4 v[84:87], v[0:7], v[48:55], v[84:87], v212, v211 op_sel_hi:[0,0,0]
	v_mfma_scale_f32_16x16x128_f8f6f4 v[76:79], v[8:15], v[56:63], v[76:79], v212, v211 op_sel_hi:[0,0,0]
	v_mfma_scale_f32_16x16x128_f8f6f4 v[68:71], v[0:7], v[56:63], v[68:71], v212, v211 op_sel_hi:[0,0,0]
	s_setprio 0
	s_barrier
; #define PG8_STAGE(bufoff, gbase, voff) do { _Pragma("unroll") for (int _i = 0; _i < 2; ++_i) { unsigned keep_; \
;         asm volatile("s_mov_b32 %0, m0\n\ts_mov_b32 m0, %3\n\ts_nop 0\n\tglobal_load_lds_dwordx4 %1, %2\n\ts_mov_b32 m0, %0" : "=&s"(keep_) : "v"((voff)[_i]), "s"((const char*)(gbase)), "s"(ldsb + (unsigned)((bufoff) + _i * 8192)) : "memory"); } } while (0)
; #define PG8_LDA(dst, b, h) do { _Pragma("unroll") for (int m = 0; m < 4; ++m) _Pragma("unroll") for (int k = 0; k < 2; ++k) dst[m][k] = *(const PG8_LAS bf16x8*)(lds + PG8_SA(b, h) + aoff + m * 2048 + k * 1024); } while (0)
; #define PG8_LDB(dst, b, h) do { _Pragma("unroll") for (int n = 0; n < 2; ++n) _Pragma("unroll") for (int k = 0; k < 2; ++k) dst[n][k] = *(const PG8_LAS bf16x8*)(lds + PG8_SB(b, h) + boff + n * 2048 + k * 1024); } while (0)
; #define PG8_WAIT_V(n) asm volatile("s_waitcnt vmcnt(" #n ")" ::: "memory")
; #define PG8_WAIT_L(n) asm volatile("s_waitcnt lgkmcnt(" #n ")" ::: "memory")
; #define PG8_BAR __builtin_amdgcn_s_barrier()
; #define PG8_SCHED __builtin_amdgcn_sched_barrier(0)
; template <class Epi, class Sched, bool ALIGN_EPI, bool FP8 = false>
; __device__ __forceinline__ void gemm_phase(PG8_LAS unsigned char* lds, const Gemm g, const Sched& S, const Epi& E, const int wid, const int lane) {
;     ...
;             PG8_LDB(B0, 1, 0); PG8_LDB(B1, 1, 1); PG8_SCHED; PG8_LDA(At, 1, 0); PG8_STAGE(PG8_SA(0, 1), a2 + hstepA, vc1);
;             PG8_WAIT_V(8); PG8_WAIT_L(0); PG8_BAR; PG8_MMA(0, 0, At, B0); PG8_MMA(0, 1, At, B1); PG8_BAR; PG8_SCHED;
;             PG8_LDA(At, 1, 1); PG8_STAGE(PG8_SB(1, 0), b3, voffB); PG8_STAGE(PG8_SB(1, 1), b3 + hstep, voffB); PG8_STAGE(PG8_SA(1, 0), a3, vc0);
;             PG8_WAIT_V(8); PG8_WAIT_L(0); PG8_BAR; PG8_MMA(1, 0, At, B0); PG8_MMA(1, 1, At, B1); PG8_BAR; PG8_SCHED;
;         }
	v_add_u32_e32 v12, 0x18000, v206
	v_add_u32_e32 v28, 0x1c000, v206
	ds_read_b128 v[0:3], v12
	ds_read_b128 v[4:7], v12 offset:1024
	ds_read_b128 v[8:11], v12 offset:2048
	ds_read_b128 v[12:15], v12 offset:3072
	ds_read_b128 v[16:19], v28
	ds_read_b128 v[20:23], v28 offset:1024
	ds_read_b128 v[24:27], v28 offset:2048
	ds_read_b128 v[28:31], v28 offset:3072
	ds_read_b128 v[32:35], v209 offset:32768
	ds_read_b128 v[36:39], v209 offset:33792
	ds_read_b128 v[40:43], v209 offset:34816
	ds_read_b128 v[44:47], v209 offset:35840
	ds_read_b128 v[48:51], v209 offset:36864
	ds_read_b128 v[52:55], v209 offset:37888
	ds_read_b128 v[56:59], v209 offset:38912
	ds_read_b128 v[60:63], v209 offset:39936
	s_mov_b32 m0, s66
	s_nop 0
	global_load_lds_dwordx4 v66, s[40:41]
	s_mov_b32 m0, s67
	s_nop 0
	global_load_lds_dwordx4 v67, s[40:41]
	s_waitcnt vmcnt(8)
	s_waitcnt lgkmcnt(0)
	s_barrier
	s_setprio 1
	s_waitcnt lgkmcnt(6)
	v_mfma_scale_f32_16x16x128_f8f6f4 v[192:195], v[0:7], v[32:39], v[192:195], v210, v211 op_sel_hi:[0,0,0]
	v_mfma_scale_f32_16x16x128_f8f6f4 v[184:187], v[8:15], v[32:39], v[184:187], v210, v211 op_sel_hi:[0,0,0]
	s_waitcnt lgkmcnt(4)
	v_mfma_scale_f32_16x16x128_f8f6f4 v[176:179], v[0:7], v[40:47], v[176:179], v210, v211 op_sel_hi:[0,0,0]
	v_mfma_scale_f32_16x16x128_f8f6f4 v[168:171], v[8:15], v[40:47], v[168:171], v210, v211 op_sel_hi:[0,0,0]
	s_waitcnt lgkmcnt(2)
	v_mfma_scale_f32_16x16x128_f8f6f4 v[160:163], v[0:7], v[48:55], v[160:163], v210, v211 op_sel_hi:[0,0,0]
	v_mfma_scale_f32_16x16x128_f8f6f4 v[152:155], v[8:15], v[48:55], v[152:155], v210, v211 op_sel_hi:[0,0,0]
	s_waitcnt lgkmcnt(0)
	v_mfma_scale_f32_16x16x128_f8f6f4 v[144:147], v[0:7], v[56:63], v[144:147], v210, v211 op_sel_hi:[0,0,0]
	v_mfma_scale_f32_16x16x128_f8f6f4 v[136:139], v[8:15], v[56:63], v[136:139], v210, v211 op_sel_hi:[0,0,0]
	s_setprio 0
	s_setprio 1
	v_mfma_scale_f32_16x16x128_f8f6f4 v[188:191], v[16:23], v[32:39], v[188:191], v212, v211 op_sel_hi:[0,0,0]
	v_mfma_scale_f32_16x16x128_f8f6f4 v[180:183], v[24:31], v[32:39], v[180:183], v212, v211 op_sel_hi:[0,0,0]
	v_mfma_scale_f32_16x16x128_f8f6f4 v[172:175], v[16:23], v[40:47], v[172:175], v212, v211 op_sel_hi:[0,0,0]
	v_mfma_scale_f32_16x16x128_f8f6f4 v[164:167], v[24:31], v[40:47], v[164:167], v212, v211 op_sel_hi:[0,0,0]
	v_mfma_scale_f32_16x16x128_f8f6f4 v[156:159], v[16:23], v[48:55], v[156:159], v212, v211 op_sel_hi:[0,0,0]
	v_mfma_scale_f32_16x16x128_f8f6f4 v[148:151], v[24:31], v[48:55], v[148:151], v212, v211 op_sel_hi:[0,0,0]
	v_mfma_scale_f32_16x16x128_f8f6f4 v[140:143], v[16:23], v[56:63], v[140:143], v212, v211 op_sel_hi:[0,0,0]
	v_mfma_scale_f32_16x16x128_f8f6f4 v[132:135], v[24:31], v[56:63], v[132:135], v212, v211 op_sel_hi:[0,0,0]
	s_setprio 0
	s_barrier
	ds_read_b128 v[32:35], v209 offset:49152
	ds_read_b128 v[36:39], v209 offset:50176
	ds_read_b128 v[40:43], v209 offset:51200
	ds_read_b128 v[44:47], v209 offset:52224
	ds_read_b128 v[48:51], v209 offset:53248
	ds_read_b128 v[52:55], v209 offset:54272
	ds_read_b128 v[56:59], v209 offset:55296
	ds_read_b128 v[60:63], v209 offset:56320
	s_mov_b32 m0, s69
	s_nop 0
	global_load_lds_dwordx4 v200, s[38:39]
	s_mov_b32 m0, s70
	s_nop 0
	global_load_lds_dwordx4 v202, s[38:39]
	s_add_u32 s38, s38, s16
	s_addc_u32 s39, s39, s17
	s_mov_b32 m0, s73
	s_nop 0
	global_load_lds_dwordx4 v200, s[38:39]
	s_mov_b32 m0, s74
	s_nop 0
	global_load_lds_dwordx4 v202, s[38:39]
	s_mov_b32 m0, s71
	s_nop 0
	global_load_lds_dwordx4 v64, s[8:9]
	s_mov_b32 m0, s72
	s_nop 0
	global_load_lds_dwordx4 v65, s[8:9]
	s_waitcnt vmcnt(8)
	s_waitcnt lgkmcnt(0)
	s_barrier
	s_setprio 1
	s_waitcnt lgkmcnt(6)
	v_mfma_scale_f32_16x16x128_f8f6f4 v[128:131], v[0:7], v[32:39], v[128:131], v210, v211 op_sel_hi:[0,0,0]
	v_mfma_scale_f32_16x16x128_f8f6f4 v[120:123], v[8:15], v[32:39], v[120:123], v210, v211 op_sel_hi:[0,0,0]
	s_waitcnt lgkmcnt(4)
	v_mfma_scale_f32_16x16x128_f8f6f4 v[112:115], v[0:7], v[40:47], v[112:115], v210, v211 op_sel_hi:[0,0,0]
	v_mfma_scale_f32_16x16x128_f8f6f4 v[104:107], v[8:15], v[40:47], v[104:107], v210, v211 op_sel_hi:[0,0,0]
	s_waitcnt lgkmcnt(2)
	v_mfma_scale_f32_16x16x128_f8f6f4 v[96:99], v[0:7], v[48:55], v[96:99], v210, v211 op_sel_hi:[0,0,0]
	v_mfma_scale_f32_16x16x128_f8f6f4 v[88:91], v[8:15], v[48:55], v[88:91], v210, v211 op_sel_hi:[0,0,0]
	s_waitcnt lgkmcnt(0)
	v_mfma_scale_f32_16x16x128_f8f6f4 v[80:83], v[0:7], v[56:63], v[80:83], v210, v211 op_sel_hi:[0,0,0]
	v_mfma_scale_f32_16x16x128_f8f6f4 v[72:75], v[8:15], v[56:63], v[72:75], v210, v211 op_sel_hi:[0,0,0]
	s_setprio 0
	s_setprio 1
	v_mfma_scale_f32_16x16x128_f8f6f4 v[124:127], v[16:23], v[32:39], v[124:127], v212, v211 op_sel_hi:[0,0,0]
	v_mfma_scale_f32_16x16x128_f8f6f4 v[116:119], v[24:31], v[32:39], v[116:119], v212, v211 op_sel_hi:[0,0,0]
	v_mfma_scale_f32_16x16x128_f8f6f4 v[108:111], v[16:23], v[40:47], v[108:111], v212, v211 op_sel_hi:[0,0,0]
	v_mfma_scale_f32_16x16x128_f8f6f4 v[100:103], v[24:31], v[40:47], v[100:103], v212, v211 op_sel_hi:[0,0,0]
	v_mfma_scale_f32_16x16x128_f8f6f4 v[92:95], v[16:23], v[48:55], v[92:95], v212, v211 op_sel_hi:[0,0,0]
	v_mfma_scale_f32_16x16x128_f8f6f4 v[84:87], v[24:31], v[48:55], v[84:87], v212, v211 op_sel_hi:[0,0,0]
	v_mfma_scale_f32_16x16x128_f8f6f4 v[76:79], v[16:23], v[56:63], v[76:79], v212, v211 op_sel_hi:[0,0,0]
	v_mfma_scale_f32_16x16x128_f8f6f4 v[68:71], v[24:31], v[56:63], v[68:71], v212, v211 op_sel_hi:[0,0,0]
	s_setprio 0
	s_barrier
	s_add_u32 s6, s6, 0x100
	s_addc_u32 s7, s7, 0
	s_cmp_ge_i32 s82, s68
	s_cbranch_scc1 .LBB0_749

; __device__ __forceinline__ unsigned pk4_fp8(float a, float b, float c, float d) { int r = __builtin_amdgcn_cvt_pk_fp8_f32(a, b, 0, false); r = __builtin_amdgcn_cvt_pk_fp8_f32(c, d, r, true); return (unsigned)r; }
;     __device__ __forceinline__ void operator()(const f32x4 (&acc)[2][2][4][2], const Unit& u, int wr, int wc, int fr, int fq) const {
;         const int row0 = u.pm * BM + wr * 64 + fr, col0 = (u.pn & 3) * 128 + wc * 32 + 8 * fq;
; #pragma unroll
;         for (int ai = 0; ai < 2; ++ai)
; #pragma unroll
;             for (int m = 0; m < 4; ++m) { float r[8];
; #pragma unroll
;                 for (int n = 0; n < 2; ++n)
; #pragma unroll
;                     for (int e = 0; e < 4; ++e) { const float g = acc[ai][0][m][n][e], up = acc[ai][1][m][n][e]; r[4 * n + e] = g * __builtin_amdgcn_rcpf(1.0f + __builtin_amdgcn_exp2f(-g * LOG2E)) * up * (float)(1 << ASHIFT); }
;                 v2u w; w.x = pk4_fp8(r[0], r[1], r[2], r[3]); w.y = pk4_fp8(r[4], r[5], r[6], r[7]);
;                 *(v2u*)(O + (size_t)(row0 + ai * HALF + m * 16) * EH + col0) = w; }
;     }
.LBB0_751:
	s_mov_b32 s98, 0xbfb8aa3b
	s_nop 15
	s_nop 15
	v_lshl_add_u32 v4, s88, 8, v203
	s_lshl_b32 s6, s89, 7
	s_and_b32 s6, s6, 0x180
	v_ashrrev_i32_e32 v5, 31, v4
	v_add_u32_e32 v2, s6, v205
	v_lshlrev_b64 v[0:1], 9, v[4:5]
	v_ashrrev_i32_e32 v3, 31, v2
	v_lshl_add_u64 v[0:1], s[24:25], 0, v[0:1]
	v_lshl_add_u64 v[0:1], v[0:1], 0, v[2:3]
	v_pk_mul_f32 v[228:229], v[192:193], s[98:99] op_sel_hi:[1,0]
	v_pk_mul_f32 v[230:231], v[194:195], s[98:99] op_sel_hi:[1,0]
	v_pk_mul_f32 v[232:233], v[184:185], s[98:99] op_sel_hi:[1,0]
	v_pk_mul_f32 v[234:235], v[186:187], s[98:99] op_sel_hi:[1,0]
	v_exp_f32_e32 v228, v228
	v_exp_f32_e32 v229, v229
	v_exp_f32_e32 v230, v230
	v_exp_f32_e32 v231, v231
	v_exp_f32_e32 v232, v232
	v_exp_f32_e32 v233, v233
	v_exp_f32_e32 v234, v234
	v_exp_f32_e32 v235, v235
	v_pk_add_f32 v[228:229], v[228:229], 1.0 op_sel_hi:[1,0]
	v_pk_add_f32 v[230:231], v[230:231], 1.0 op_sel_hi:[1,0]
	v_pk_add_f32 v[232:233], v[232:233], 1.0 op_sel_hi:[1,0]
	v_pk_add_f32 v[234:235], v[234:235], 1.0 op_sel_hi:[1,0]
	v_rcp_f32_e32 v228, v228
	v_rcp_f32_e32 v229, v229
	v_rcp_f32_e32 v230, v230
	v_rcp_f32_e32 v231, v231
	v_rcp_f32_e32 v232, v232
	v_rcp_f32_e32 v233, v233
	v_rcp_f32_e32 v234, v234
	v_rcp_f32_e32 v235, v235
	v_pk_mul_f32 v[228:229], v[192:193], v[228:229]
	v_pk_mul_f32 v[230:231], v[194:195], v[230:231]
	v_pk_mul_f32 v[232:233], v[184:185], v[232:233]
	v_pk_mul_f32 v[234:235], v[186:187], v[234:235]
	v_pk_mul_f32 v[228:229], v[188:189], v[228:229]
	v_pk_mul_f32 v[230:231], v[190:191], v[230:231]
	v_pk_mul_f32 v[232:233], v[180:181], v[232:233]
	v_pk_mul_f32 v[234:235], v[182:183], v[234:235]
	v_mov_b32_e32 v244, 0
	v_mov_b32_e32 v245, 0
	v_cvt_pk_fp8_f32 v244, v228, v229
	v_cvt_pk_fp8_f32 v245, v232, v233
	v_cvt_pk_fp8_f32 v244, v230, v231 op_sel:[0,0,1]
	v_cvt_pk_fp8_f32 v245, v234, v235 op_sel:[0,0,1]
	s_nop 0
	global_store_dwordx2 v[0:1], v[244:245], off
	v_or_b32_e32 v8, 16, v4
	v_ashrrev_i32_e32 v9, 31, v8
	v_lshlrev_b64 v[8:9], 9, v[8:9]
	v_lshl_add_u64 v[8:9], s[24:25], 0, v[8:9]
	v_lshl_add_u64 v[8:9], v[8:9], 0, v[2:3]
	v_pk_mul_f32 v[228:229], v[176:177], s[98:99] op_sel_hi:[1,0]
	v_pk_mul_f32 v[230:231], v[178:179], s[98:99] op_sel_hi:[1,0]
	v_pk_mul_f32 v[232:233], v[168:169], s[98:99] op_sel_hi:[1,0]
	v_pk_mul_f32 v[234:235], v[170:171], s[98:99] op_sel_hi:[1,0]
	v_exp_f32_e32 v228, v228
	v_exp_f32_e32 v229, v229
	v_exp_f32_e32 v230, v230
	v_exp_f32_e32 v231, v231
	v_exp_f32_e32 v232, v232
	v_exp_f32_e32 v233, v233
	v_exp_f32_e32 v234, v234
	v_exp_f32_e32 v235, v235
	v_pk_add_f32 v[228:229], v[228:229], 1.0 op_sel_hi:[1,0]
	v_pk_add_f32 v[230:231], v[230:231], 1.0 op_sel_hi:[1,0]
	v_pk_add_f32 v[232:233], v[232:233], 1.0 op_sel_hi:[1,0]
	v_pk_add_f32 v[234:235], v[234:235], 1.0 op_sel_hi:[1,0]
	v_rcp_f32_e32 v228, v228
	v_rcp_f32_e32 v229, v229
	v_rcp_f32_e32 v230, v230
	v_rcp_f32_e32 v231, v231
	v_rcp_f32_e32 v232, v232
	v_rcp_f32_e32 v233, v233
	v_rcp_f32_e32 v234, v234
	v_rcp_f32_e32 v235, v235
	v_pk_mul_f32 v[228:229], v[176:177], v[228:229]
	v_pk_mul_f32 v[230:231], v[178:179], v[230:231]
	v_pk_mul_f32 v[232:233], v[168:169], v[232:233]
	v_pk_mul_f32 v[234:235], v[170:171], v[234:235]
	v_pk_mul_f32 v[228:229], v[172:173], v[228:229]
	v_pk_mul_f32 v[230:231], v[174:175], v[230:231]
	v_pk_mul_f32 v[232:233], v[164:165], v[232:233]
	v_pk_mul_f32 v[234:235], v[166:167], v[234:235]
	v_mov_b32_e32 v244, 0
	v_mov_b32_e32 v245, 0
	v_cvt_pk_fp8_f32 v244, v228, v229
	v_cvt_pk_fp8_f32 v245, v232, v233
	v_cvt_pk_fp8_f32 v244, v230, v231 op_sel:[0,0,1]
	v_cvt_pk_fp8_f32 v245, v234, v235 op_sel:[0,0,1]
	s_nop 0
	global_store_dwordx2 v[8:9], v[244:245], off
	v_or_b32_e32 v8, 32, v4
	v_ashrrev_i32_e32 v9, 31, v8
	v_lshlrev_b64 v[8:9], 9, v[8:9]
	v_lshl_add_u64 v[8:9], s[24:25], 0, v[8:9]
	v_lshl_add_u64 v[8:9], v[8:9], 0, v[2:3]
	v_pk_mul_f32 v[228:229], v[160:161], s[98:99] op_sel_hi:[1,0]
	v_pk_mul_f32 v[230:231], v[162:163], s[98:99] op_sel_hi:[1,0]
	v_pk_mul_f32 v[232:233], v[152:153], s[98:99] op_sel_hi:[1,0]
	v_pk_mul_f32 v[234:235], v[154:155], s[98:99] op_sel_hi:[1,0]
	v_exp_f32_e32 v228, v228
	v_exp_f32_e32 v229, v229
	v_exp_f32_e32 v230, v230
	v_exp_f32_e32 v231, v231
	v_exp_f32_e32 v232, v232
	v_exp_f32_e32 v233, v233
	v_exp_f32_e32 v234, v234
	v_exp_f32_e32 v235, v235
	v_pk_add_f32 v[228:229], v[228:229], 1.0 op_sel_hi:[1,0]
	v_pk_add_f32 v[230:231], v[230:231], 1.0 op_sel_hi:[1,0]
	v_pk_add_f32 v[232:233], v[232:233], 1.0 op_sel_hi:[1,0]
	v_pk_add_f32 v[234:235], v[234:235], 1.0 op_sel_hi:[1,0]
	v_rcp_f32_e32 v228, v228
	v_rcp_f32_e32 v229, v229
	v_rcp_f32_e32 v230, v230
	v_rcp_f32_e32 v231, v231
	v_rcp_f32_e32 v232, v232
	v_rcp_f32_e32 v233, v233
	v_rcp_f32_e32 v234, v234
	v_rcp_f32_e32 v235, v235
	v_pk_mul_f32 v[228:229], v[160:161], v[228:229]
	v_pk_mul_f32 v[230:231], v[162:163], v[230:231]
	v_pk_mul_f32 v[232:233], v[152:153], v[232:233]
	v_pk_mul_f32 v[234:235], v[154:155], v[234:235]
	v_pk_mul_f32 v[228:229], v[156:157], v[228:229]
	v_pk_mul_f32 v[230:231], v[158:159], v[230:231]
	v_pk_mul_f32 v[232:233], v[148:149], v[232:233]
	v_pk_mul_f32 v[234:235], v[150:151], v[234:235]
	v_mov_b32_e32 v244, 0
	v_mov_b32_e32 v245, 0
	v_cvt_pk_fp8_f32 v244, v228, v229
	v_cvt_pk_fp8_f32 v245, v232, v233
	v_cvt_pk_fp8_f32 v244, v230, v231 op_sel:[0,0,1]
	v_cvt_pk_fp8_f32 v245, v234, v235 op_sel:[0,0,1]
	s_nop 0
	global_store_dwordx2 v[8:9], v[244:245], off
	v_or_b32_e32 v4, 48, v4
	v_ashrrev_i32_e32 v5, 31, v4
	v_lshlrev_b64 v[4:5], 9, v[4:5]
	v_lshl_add_u64 v[4:5], s[24:25], 0, v[4:5]
	v_lshl_add_u64 v[2:3], v[4:5], 0, v[2:3]
	v_pk_mul_f32 v[228:229], v[144:145], s[98:99] op_sel_hi:[1,0]
; __device__ __forceinline__ unsigned pk4_fp8(float a, float b, float c, float d) { int r = __builtin_amdgcn_cvt_pk_fp8_f32(a, b, 0, false); r = __builtin_amdgcn_cvt_pk_fp8_f32(c, d, r, true); return (unsigned)r; }
;     __device__ __forceinline__ void operator()(const f32x4 (&acc)[2][2][4][2], const Unit& u, int wr, int wc, int fr, int fq) const {
;         const int row0 = u.pm * BM + wr * 64 + fr, col0 = (u.pn & 3) * 128 + wc * 32 + 8 * fq;
; #pragma unroll
;         for (int ai = 0; ai < 2; ++ai)
; #pragma unroll
;             for (int m = 0; m < 4; ++m) { float r[8];
; #pragma unroll
;                 for (int n = 0; n < 2; ++n)
; #pragma unroll
;                     for (int e = 0; e < 4; ++e) { const float g = acc[ai][0][m][n][e], up = acc[ai][1][m][n][e]; r[4 * n + e] = g * __builtin_amdgcn_rcpf(1.0f + __builtin_amdgcn_exp2f(-g * LOG2E)) * up * (float)(1 << ASHIFT); }
;                 v2u w; w.x = pk4_fp8(r[0], r[1], r[2], r[3]); w.y = pk4_fp8(r[4], r[5], r[6], r[7]);
;                 *(v2u*)(O + (size_t)(row0 + ai * HALF + m * 16) * EH + col0) = w; }
;     }
	v_pk_mul_f32 v[230:231], v[146:147], s[98:99] op_sel_hi:[1,0]
	v_pk_mul_f32 v[232:233], v[136:137], s[98:99] op_sel_hi:[1,0]
	v_pk_mul_f32 v[234:235], v[138:139], s[98:99] op_sel_hi:[1,0]
	v_exp_f32_e32 v228, v228
	v_exp_f32_e32 v229, v229
	v_exp_f32_e32 v230, v230
	v_exp_f32_e32 v231, v231
	v_exp_f32_e32 v232, v232
	v_exp_f32_e32 v233, v233
	v_exp_f32_e32 v234, v234
	v_exp_f32_e32 v235, v235
	v_pk_add_f32 v[228:229], v[228:229], 1.0 op_sel_hi:[1,0]
	v_pk_add_f32 v[230:231], v[230:231], 1.0 op_sel_hi:[1,0]
	v_pk_add_f32 v[232:233], v[232:233], 1.0 op_sel_hi:[1,0]
	v_pk_add_f32 v[234:235], v[234:235], 1.0 op_sel_hi:[1,0]
	v_rcp_f32_e32 v228, v228
	v_rcp_f32_e32 v229, v229
	v_rcp_f32_e32 v230, v230
	v_rcp_f32_e32 v231, v231
	v_rcp_f32_e32 v232, v232
	v_rcp_f32_e32 v233, v233
	v_rcp_f32_e32 v234, v234
	v_rcp_f32_e32 v235, v235
	v_pk_mul_f32 v[228:229], v[144:145], v[228:229]
	v_pk_mul_f32 v[230:231], v[146:147], v[230:231]
	v_pk_mul_f32 v[232:233], v[136:137], v[232:233]
	v_pk_mul_f32 v[234:235], v[138:139], v[234:235]
	v_pk_mul_f32 v[228:229], v[140:141], v[228:229]
	v_pk_mul_f32 v[230:231], v[142:143], v[230:231]
	v_pk_mul_f32 v[232:233], v[132:133], v[232:233]
	v_pk_mul_f32 v[234:235], v[134:135], v[234:235]
	v_mov_b32_e32 v244, 0
	v_mov_b32_e32 v245, 0
	v_cvt_pk_fp8_f32 v244, v228, v229
	v_cvt_pk_fp8_f32 v245, v232, v233
	v_cvt_pk_fp8_f32 v244, v230, v231 op_sel:[0,0,1]
	v_cvt_pk_fp8_f32 v245, v234, v235 op_sel:[0,0,1]
	s_nop 0
	global_store_dwordx2 v[2:3], v[244:245], off
	v_add_co_u32_e32 v4, vcc, s50, v0
	s_nop 0
	v_addc_co_u32_e32 v5, vcc, 0, v1, vcc
	v_pk_mul_f32 v[228:229], v[128:129], s[98:99] op_sel_hi:[1,0]
	v_pk_mul_f32 v[230:231], v[130:131], s[98:99] op_sel_hi:[1,0]
	v_pk_mul_f32 v[232:233], v[120:121], s[98:99] op_sel_hi:[1,0]
	v_pk_mul_f32 v[234:235], v[122:123], s[98:99] op_sel_hi:[1,0]
	v_exp_f32_e32 v228, v228
	v_exp_f32_e32 v229, v229
	v_exp_f32_e32 v230, v230
	v_exp_f32_e32 v231, v231
	v_exp_f32_e32 v232, v232
	v_exp_f32_e32 v233, v233
	v_exp_f32_e32 v234, v234
	v_exp_f32_e32 v235, v235
	v_pk_add_f32 v[228:229], v[228:229], 1.0 op_sel_hi:[1,0]
	v_pk_add_f32 v[230:231], v[230:231], 1.0 op_sel_hi:[1,0]
	v_pk_add_f32 v[232:233], v[232:233], 1.0 op_sel_hi:[1,0]
	v_pk_add_f32 v[234:235], v[234:235], 1.0 op_sel_hi:[1,0]
	v_rcp_f32_e32 v228, v228
	v_rcp_f32_e32 v229, v229
	v_rcp_f32_e32 v230, v230
	v_rcp_f32_e32 v231, v231
	v_rcp_f32_e32 v232, v232
	v_rcp_f32_e32 v233, v233
	v_rcp_f32_e32 v234, v234
	v_rcp_f32_e32 v235, v235
	v_pk_mul_f32 v[228:229], v[128:129], v[228:229]
	v_pk_mul_f32 v[230:231], v[130:131], v[230:231]
	v_pk_mul_f32 v[232:233], v[120:121], v[232:233]
	v_pk_mul_f32 v[234:235], v[122:123], v[234:235]
	v_pk_mul_f32 v[228:229], v[124:125], v[228:229]
	v_pk_mul_f32 v[230:231], v[126:127], v[230:231]
	v_pk_mul_f32 v[232:233], v[116:117], v[232:233]
	v_pk_mul_f32 v[234:235], v[118:119], v[234:235]
	v_mov_b32_e32 v244, 0
	v_mov_b32_e32 v245, 0
	v_cvt_pk_fp8_f32 v244, v228, v229
	v_cvt_pk_fp8_f32 v245, v232, v233
	v_cvt_pk_fp8_f32 v244, v230, v231 op_sel:[0,0,1]
	v_cvt_pk_fp8_f32 v245, v234, v235 op_sel:[0,0,1]
	s_nop 0
	global_store_dwordx2 v[4:5], v[244:245], off
	v_add_co_u32_e32 v4, vcc, s52, v0
	s_nop 0
	v_addc_co_u32_e32 v5, vcc, 0, v1, vcc
	v_pk_mul_f32 v[228:229], v[112:113], s[98:99] op_sel_hi:[1,0]
	v_pk_mul_f32 v[230:231], v[114:115], s[98:99] op_sel_hi:[1,0]
	v_pk_mul_f32 v[232:233], v[104:105], s[98:99] op_sel_hi:[1,0]
	v_pk_mul_f32 v[234:235], v[106:107], s[98:99] op_sel_hi:[1,0]
	v_exp_f32_e32 v228, v228
	v_exp_f32_e32 v229, v229
	v_exp_f32_e32 v230, v230
	v_exp_f32_e32 v231, v231
	v_exp_f32_e32 v232, v232
	v_exp_f32_e32 v233, v233
	v_exp_f32_e32 v234, v234
	v_exp_f32_e32 v235, v235
	v_pk_add_f32 v[228:229], v[228:229], 1.0 op_sel_hi:[1,0]
	v_pk_add_f32 v[230:231], v[230:231], 1.0 op_sel_hi:[1,0]
	v_pk_add_f32 v[232:233], v[232:233], 1.0 op_sel_hi:[1,0]
	v_pk_add_f32 v[234:235], v[234:235], 1.0 op_sel_hi:[1,0]
	v_rcp_f32_e32 v228, v228
	v_rcp_f32_e32 v229, v229
	v_rcp_f32_e32 v230, v230
	v_rcp_f32_e32 v231, v231
	v_rcp_f32_e32 v232, v232
	v_rcp_f32_e32 v233, v233
	v_rcp_f32_e32 v234, v234
; __device__ __forceinline__ unsigned pk4_fp8(float a, float b, float c, float d) { int r = __builtin_amdgcn_cvt_pk_fp8_f32(a, b, 0, false); r = __builtin_amdgcn_cvt_pk_fp8_f32(c, d, r, true); return (unsigned)r; }
;     __device__ __forceinline__ void operator()(const f32x4 (&acc)[2][2][4][2], const Unit& u, int wr, int wc, int fr, int fq) const {
;         const int row0 = u.pm * BM + wr * 64 + fr, col0 = (u.pn & 3) * 128 + wc * 32 + 8 * fq;
; #pragma unroll
;         for (int ai = 0; ai < 2; ++ai)
; #pragma unroll
;             for (int m = 0; m < 4; ++m) { float r[8];
; #pragma unroll
;                 for (int n = 0; n < 2; ++n)
; #pragma unroll
;                     for (int e = 0; e < 4; ++e) { const float g = acc[ai][0][m][n][e], up = acc[ai][1][m][n][e]; r[4 * n + e] = g * __builtin_amdgcn_rcpf(1.0f + __builtin_amdgcn_exp2f(-g * LOG2E)) * up * (float)(1 << ASHIFT); }
;                 v2u w; w.x = pk4_fp8(r[0], r[1], r[2], r[3]); w.y = pk4_fp8(r[4], r[5], r[6], r[7]);
;                 *(v2u*)(O + (size_t)(row0 + ai * HALF + m * 16) * EH + col0) = w; }
;     }
	v_rcp_f32_e32 v235, v235
	v_pk_mul_f32 v[228:229], v[112:113], v[228:229]
	v_pk_mul_f32 v[230:231], v[114:115], v[230:231]
	v_pk_mul_f32 v[232:233], v[104:105], v[232:233]
	v_pk_mul_f32 v[234:235], v[106:107], v[234:235]
	v_pk_mul_f32 v[228:229], v[108:109], v[228:229]
	v_pk_mul_f32 v[230:231], v[110:111], v[230:231]
	v_pk_mul_f32 v[232:233], v[100:101], v[232:233]
	v_pk_mul_f32 v[234:235], v[102:103], v[234:235]
	v_mov_b32_e32 v244, 0
	v_mov_b32_e32 v245, 0
	v_cvt_pk_fp8_f32 v244, v228, v229
	v_cvt_pk_fp8_f32 v245, v232, v233
	v_cvt_pk_fp8_f32 v244, v230, v231 op_sel:[0,0,1]
	v_cvt_pk_fp8_f32 v245, v234, v235 op_sel:[0,0,1]
	s_nop 0
	global_store_dwordx2 v[4:5], v[244:245], off
	v_add_co_u32_e32 v4, vcc, s54, v0
	s_nop 0
	v_addc_co_u32_e32 v5, vcc, 0, v1, vcc
	v_pk_mul_f32 v[228:229], v[96:97], s[98:99] op_sel_hi:[1,0]
	v_pk_mul_f32 v[230:231], v[98:99], s[98:99] op_sel_hi:[1,0]
	v_pk_mul_f32 v[232:233], v[88:89], s[98:99] op_sel_hi:[1,0]
	v_pk_mul_f32 v[234:235], v[90:91], s[98:99] op_sel_hi:[1,0]
	v_exp_f32_e32 v228, v228
	v_exp_f32_e32 v229, v229
	v_exp_f32_e32 v230, v230
	v_exp_f32_e32 v231, v231
	v_exp_f32_e32 v232, v232
	v_exp_f32_e32 v233, v233
	v_exp_f32_e32 v234, v234
	v_exp_f32_e32 v235, v235
	v_pk_add_f32 v[228:229], v[228:229], 1.0 op_sel_hi:[1,0]
	v_pk_add_f32 v[230:231], v[230:231], 1.0 op_sel_hi:[1,0]
	v_pk_add_f32 v[232:233], v[232:233], 1.0 op_sel_hi:[1,0]
	v_pk_add_f32 v[234:235], v[234:235], 1.0 op_sel_hi:[1,0]
	v_rcp_f32_e32 v228, v228
	v_rcp_f32_e32 v229, v229
	v_rcp_f32_e32 v230, v230
	v_rcp_f32_e32 v231, v231
	v_rcp_f32_e32 v232, v232
	v_rcp_f32_e32 v233, v233
	v_rcp_f32_e32 v234, v234
	v_rcp_f32_e32 v235, v235
	v_pk_mul_f32 v[228:229], v[96:97], v[228:229]
	v_pk_mul_f32 v[230:231], v[98:99], v[230:231]
	v_pk_mul_f32 v[232:233], v[88:89], v[232:233]
	v_pk_mul_f32 v[234:235], v[90:91], v[234:235]
	v_pk_mul_f32 v[228:229], v[92:93], v[228:229]
	v_pk_mul_f32 v[230:231], v[94:95], v[230:231]
	v_pk_mul_f32 v[232:233], v[84:85], v[232:233]
	v_pk_mul_f32 v[234:235], v[86:87], v[234:235]
	v_mov_b32_e32 v244, 0
	v_mov_b32_e32 v245, 0
	v_cvt_pk_fp8_f32 v244, v228, v229
	v_cvt_pk_fp8_f32 v245, v232, v233
	v_cvt_pk_fp8_f32 v244, v230, v231 op_sel:[0,0,1]
	v_cvt_pk_fp8_f32 v245, v234, v235 op_sel:[0,0,1]
	s_nop 0
	global_store_dwordx2 v[4:5], v[244:245], off
	v_add_co_u32_e32 v0, vcc, 0x16000, v0
	s_nop 1
	v_addc_co_u32_e32 v1, vcc, 0, v1, vcc
	s_and_b64 vcc, exec, s[4:5]
	s_mov_b64 s[4:5], -1
	v_pk_mul_f32 v[228:229], v[80:81], s[98:99] op_sel_hi:[1,0]
	v_pk_mul_f32 v[230:231], v[82:83], s[98:99] op_sel_hi:[1,0]
	v_pk_mul_f32 v[232:233], v[72:73], s[98:99] op_sel_hi:[1,0]
	v_pk_mul_f32 v[234:235], v[74:75], s[98:99] op_sel_hi:[1,0]
	v_exp_f32_e32 v228, v228
	v_exp_f32_e32 v229, v229
	v_exp_f32_e32 v230, v230
	v_exp_f32_e32 v231, v231
	v_exp_f32_e32 v232, v232
	v_exp_f32_e32 v233, v233
	v_exp_f32_e32 v234, v234
	v_exp_f32_e32 v235, v235
	v_pk_add_f32 v[228:229], v[228:229], 1.0 op_sel_hi:[1,0]
	v_pk_add_f32 v[230:231], v[230:231], 1.0 op_sel_hi:[1,0]
	v_pk_add_f32 v[232:233], v[232:233], 1.0 op_sel_hi:[1,0]
	v_pk_add_f32 v[234:235], v[234:235], 1.0 op_sel_hi:[1,0]
	v_rcp_f32_e32 v228, v228
	v_rcp_f32_e32 v229, v229
	v_rcp_f32_e32 v230, v230
	v_rcp_f32_e32 v231, v231
	v_rcp_f32_e32 v232, v232
	v_rcp_f32_e32 v233, v233
	v_rcp_f32_e32 v234, v234
	v_rcp_f32_e32 v235, v235
	v_pk_mul_f32 v[228:229], v[80:81], v[228:229]
	v_pk_mul_f32 v[230:231], v[82:83], v[230:231]
	v_pk_mul_f32 v[232:233], v[72:73], v[232:233]
	v_pk_mul_f32 v[234:235], v[74:75], v[234:235]
	v_pk_mul_f32 v[228:229], v[76:77], v[228:229]
	v_pk_mul_f32 v[230:231], v[78:79], v[230:231]
	v_pk_mul_f32 v[232:233], v[68:69], v[232:233]
	v_pk_mul_f32 v[234:235], v[70:71], v[234:235]
	v_mov_b32_e32 v244, 0
	v_mov_b32_e32 v245, 0
	v_cvt_pk_fp8_f32 v244, v228, v229
	v_cvt_pk_fp8_f32 v245, v232, v233
	v_cvt_pk_fp8_f32 v244, v230, v231 op_sel:[0,0,1]
	v_cvt_pk_fp8_f32 v245, v234, v235 op_sel:[0,0,1]
	s_nop 0
	global_store_dwordx2 v[0:1], v[244:245], off
	s_cbranch_vccnz .LBB0_715
	s_andn2_b64 vcc, exec, s[22:23]
	s_cbranch_vccnz .LBB0_714
	s_barrier
	s_branch .LBB0_714

; #define PG8_STAGE(bufoff, gbase, voff) do { _Pragma("unroll") for (int _i = 0; _i < 2; ++_i) { unsigned keep_; \
;         asm volatile("s_mov_b32 %0, m0\n\ts_mov_b32 m0, %3\n\ts_nop 0\n\tglobal_load_lds_dwordx4 %1, %2\n\ts_mov_b32 m0, %0" : "=&s"(keep_) : "v"((voff)[_i]), "s"((const char*)(gbase)), "s"(ldsb + (unsigned)((bufoff) + _i * 8192)) : "memory"); } } while (0)
; #define PG8_WAIT_V(n) asm volatile("s_waitcnt vmcnt(" #n ")" ::: "memory")
; #define PG8_BAR __builtin_amdgcn_s_barrier()
; template <class Epi, class Sched, bool ALIGN_EPI, bool FP8 = false>
; __device__ __forceinline__ void gemm_phase(PG8_LAS unsigned char* lds, const Gemm g, const Sched& S, const Epi& E, const int wid, const int lane) {
;     ...
;     const int tid = wid * 64 + lane, wr = wid >> 2, wc = wid & 3, fr = lane & 15, fq = lane >> 4;
;     int KB = g.KB; asm volatile("" : "+s"(KB)); const int nt = KB / 128;
;     unsigned voffA[2], voffB[2]; int rA[2]; unsigned cA2[2];
; #pragma unroll
;     for (int i = 0; i < 2; ++i) { int R, C; stage_rc(tid * 16 + i * 8192, R, C); const int Rb = Epi::PERM ? ((R & ~31) + perm32(R & 31)) : R;
;         rA[i] = R; cA2[i] = (unsigned)C * 2u; voffA[i] = (unsigned)(R * KB + C * 2); voffB[i] = (unsigned)(Rb * KB + C * 2); }
;     const size_t kstep = (size_t)(BK * 2);
;     const size_t hstep = (size_t)HALF * KB;
;     const size_t hstepA = GA ? (size_t)0 : hstep;
;     const size_t tstep = 2 * hstep;
;     const unsigned ldsw = (unsigned)wid * 1024u;
;     const int aoff = lds_byte(wr * 64 + fr, fq * 8), boff = lds_byte(wc * 32 + fr, fq * 8);
;     ...
;     const unsigned ldsb = (unsigned)__builtin_amdgcn_readfirstlane((int)((unsigned)(__UINTPTR_TYPE__)lds + ldsw));
;     ...
;     const char* cA = GA ? (const char*)g.A : (const char*)g.A + (size_t)cur.pm * tstep; const char* cB = (const char*)g.Bt + (size_t)cur.pn * tstep;
;     PG8_STAGE(PG8_SB(0, 0), cB, voffB); PG8_STAGE(PG8_SB(0, 1), cB + hstep, voffB); PG8_STAGE(PG8_SA(0, 0), cA, vc0); PG8_STAGE(PG8_SA(0, 1), cA + hstepA, vc1);
;     if (wr == 1) PG8_BAR;
;     PG8_WAIT_V(2); PG8_BAR;
;     PG8_STAGE(PG8_SB(1, 0), cB + kstep, voffB); PG8_STAGE(PG8_SA(1, 0), cA + kstep, vc0); PG8_STAGE(PG8_SB(1, 1), cB + hstep + kstep, voffB);
;     PG8_WAIT_V(6); PG8_BAR;
.LBB0_1623:
	v_and_b32_e32 v0, 15, v10
	s_add_i32 s5, 0, 0x21800
	v_lshl_or_b32 v203, s4, 6, v0
	v_ashrrev_i32_e32 v2, 6, v10
	s_lshl_b32 s4, s4, 13
	v_lshl_add_u32 v201, v197, 4, s5
	s_lshr_b32 s5, s9, 25
	v_lshl_add_u32 v4, v2, 10, s4
	s_lshl_b32 s4, s80, 5
	s_add_i32 s5, s8, s5
	s_and_b32 s9, s4, 0x60
	s_ashr_i32 s68, s5, 7
	s_lshr_b32 s4, s9, 3
	s_add_u32 s24, s56, 0x45c00000
	s_addc_u32 s25, s57, 0
	v_add_lshl_u32 v2, v2, s4, 10
	s_add_u32 s4, s56, 0x41c00080
	s_addc_u32 s5, s57, 0
	s_add_u32 s26, s34, 0x80
	s_waitcnt vmcnt(2)
	s_barrier
	s_addc_u32 s27, s35, 0
	s_add_i32 s69, s47, 0x18000
	s_mov_b32 m0, s69
	s_nop 0
	global_load_lds_dwordx4 v200, s[26:27]
	s_add_i32 s70, s47, 0x1a000
	s_add_i32 s71, s47, 0x8000
	s_add_i32 s72, s47, 0xa000
	s_mov_b32 m0, s70
	s_nop 0
	global_load_lds_dwordx4 v202, s[26:27]
	s_add_u32 s0, s0, 0x80
	s_mov_b32 m0, s71
	s_nop 0
	global_load_lds_dwordx4 v64, s[4:5]
	s_addc_u32 s1, s1, 0
	s_add_i32 s73, s47, 0x1c000
	s_add_i32 s74, s47, 0x1e000
	v_and_b32_e32 v3, 48, v10
	s_mov_b32 m0, s72
	s_nop 0
	global_load_lds_dwordx4 v65, s[4:5]
	s_cmpk_gt_i32 s8, 0x7f
	v_lshl_or_b32 v0, v0, 6, v3
	v_lshlrev_b32_e32 v3, 2, v10
	s_mov_b32 m0, s73
	s_nop 0
	global_load_lds_dwordx4 v200, s[0:1]
	s_cselect_b64 s[26:27], -1, 0
	s_add_i32 s75, s68, -2
	s_add_i32 s82, s47, 0xc000
	v_ashrrev_i32_e32 v1, 1, v10
	v_and_b32_e32 v3, 32, v3
	s_mov_b32 m0, s74
	s_nop 0
	global_load_lds_dwordx4 v202, s[0:1]
	s_cmpk_lt_u32 s90, 0x100
	v_and_b32_e32 v1, -8, v1
	v_bitop3_b32 v4, v0, v4, v3 bitop3:0xde
	v_bitop3_b32 v0, v0, v2, v3 bitop3:0xde
	s_waitcnt vmcnt(6)
	s_cselect_b64 s[28:29], -1, 0
	s_ashr_i32 s0, s76, 3
	v_add_u32_e32 v205, s9, v1
	s_mul_i32 s84, s0, s3
	v_cndmask_b32_e64 v1, 0, 1, s[6:7]
	v_add_u32_e32 v206, 0, v0
	s_add_i32 s83, s47, 0xe000
	s_add_i32 s84, s84, s44
	v_cmp_ne_u32_e64 s[0:1], 1, v1
	v_add_u32_e32 v207, 0x10000, v206
	v_add_u32_e32 v208, 0x14000, v206
	v_add_u32_e32 v209, 0, v4
	v_mov_b32_e32 v210, 0x79
	v_mov_b32_e32 v211, 0x7f
	v_mov_b32_e32 v212, 0x7d
	s_barrier
	s_branch .LBB0_1626

; #define PG8_STAGE(bufoff, gbase, voff) do { _Pragma("unroll") for (int _i = 0; _i < 2; ++_i) { unsigned keep_; \
;         asm volatile("s_mov_b32 %0, m0\n\ts_mov_b32 m0, %3\n\ts_nop 0\n\tglobal_load_lds_dwordx4 %1, %2\n\ts_mov_b32 m0, %0" : "=&s"(keep_) : "v"((voff)[_i]), "s"((const char*)(gbase)), "s"(ldsb + (unsigned)((bufoff) + _i * 8192)) : "memory"); } } while (0)
; #define PG8_LDA(dst, b, h) do { _Pragma("unroll") for (int m = 0; m < 4; ++m) _Pragma("unroll") for (int k = 0; k < 2; ++k) dst[m][k] = *(const PG8_LAS bf16x8*)(lds + PG8_SA(b, h) + aoff + m * 2048 + k * 1024); } while (0)
; #define PG8_LDB(dst, b, h) do { _Pragma("unroll") for (int n = 0; n < 2; ++n) _Pragma("unroll") for (int k = 0; k < 2; ++k) dst[n][k] = *(const PG8_LAS bf16x8*)(lds + PG8_SB(b, h) + boff + n * 2048 + k * 1024); } while (0)
; #define PG8_WAIT_V(n) asm volatile("s_waitcnt vmcnt(" #n ")" ::: "memory")
; #define PG8_WAIT_L(n) asm volatile("s_waitcnt lgkmcnt(" #n ")" ::: "memory")
; #define PG8_BAR __builtin_amdgcn_s_barrier()
; #define PG8_SCHED __builtin_amdgcn_sched_barrier(0)
; template <class Epi, class Sched, bool ALIGN_EPI, bool FP8 = false>
; __device__ __forceinline__ void gemm_phase(PG8_LAS unsigned char* lds, const Gemm g, const Sched& S, const Epi& E, const int wid, const int lane) {
;     ...
;         for (int t = 0; t < nt; t += 2) {
;             const bool last = (t == nt - 2);
;             const char* a1 = cA + (size_t)(t + 1) * kstep;
;             const char* a2 = last ? nA : cA + (size_t)(t + 2) * kstep; const char* b2 = last ? nB : cB + (size_t)(t + 2) * kstep;
;             const char* a3 = a2 + kstep; const char* b3 = b2 + kstep;
;             PG8_LDB(B0, 0, 0); PG8_LDB(B1, 0, 1); PG8_SCHED; PG8_LDA(At, 0, 0); PG8_STAGE(PG8_SA(1, 1), a1 + hstepA, vc1);
;             if (GA && last && has_next) { const u32x4 q = *gslot; vc0[0] = q.x; vc0[1] = q.y; vc1[0] = q.z; vc1[1] = q.w; }
;             PG8_WAIT_V(8); PG8_WAIT_L(0); PG8_BAR; PG8_MMA(0, 0, At, B0); PG8_MMA(0, 1, At, B1); PG8_BAR; PG8_SCHED;
;             PG8_LDA(At, 0, 1); PG8_STAGE(PG8_SB(0, 0), b2, voffB); PG8_STAGE(PG8_SB(0, 1), b2 + hstep, voffB); PG8_STAGE(PG8_SA(0, 0), a2, vc0);
;             PG8_WAIT_V(8); PG8_WAIT_L(0); PG8_BAR; PG8_MMA(1, 0, At, B0); PG8_MMA(1, 1, At, B1); PG8_BAR; PG8_SCHED;
.LBB0_1637:
	s_add_i32 s89, s89, 2
	s_and_b64 s[8:9], s[38:39], exec
	s_cselect_b32 s9, 0, s6
	s_cselect_b32 s8, 0, s7
	s_add_u32 s40, s20, s9
	s_addc_u32 s41, s21, s8
	s_add_u32 s33, s34, s6
	s_addc_u32 s42, s35, s7
	s_add_u32 s8, s40, 0x80
	s_addc_u32 s9, s41, 0
	s_waitcnt vmcnt(8)
	s_and_b64 s[38:39], s[38:39], exec
	s_waitcnt lgkmcnt(0)
	s_cselect_b32 s43, s31, s42
	s_cselect_b32 s42, s30, s33
	s_add_u32 s38, s42, 0x80
	s_addc_u32 s39, s43, 0
	s_barrier
	s_setprio 1
	s_waitcnt lgkmcnt(6)
	v_mfma_scale_f32_16x16x128_f8f6f4 v[192:195], v[24:31], v[56:63], v[192:195], v210, v211 op_sel_hi:[0,0,0]
	v_mfma_scale_f32_16x16x128_f8f6f4 v[184:187], v[16:23], v[56:63], v[184:187], v210, v211 op_sel_hi:[0,0,0]
	s_waitcnt lgkmcnt(4)
	v_mfma_scale_f32_16x16x128_f8f6f4 v[176:179], v[24:31], v[48:55], v[176:179], v210, v211 op_sel_hi:[0,0,0]
	v_mfma_scale_f32_16x16x128_f8f6f4 v[168:171], v[16:23], v[48:55], v[168:171], v210, v211 op_sel_hi:[0,0,0]
	s_waitcnt lgkmcnt(2)
	v_mfma_scale_f32_16x16x128_f8f6f4 v[160:163], v[24:31], v[40:47], v[160:163], v210, v211 op_sel_hi:[0,0,0]
	v_mfma_scale_f32_16x16x128_f8f6f4 v[152:155], v[16:23], v[40:47], v[152:155], v210, v211 op_sel_hi:[0,0,0]
	s_waitcnt lgkmcnt(0)
	v_mfma_scale_f32_16x16x128_f8f6f4 v[144:147], v[24:31], v[32:39], v[144:147], v210, v211 op_sel_hi:[0,0,0]
	v_mfma_scale_f32_16x16x128_f8f6f4 v[136:139], v[16:23], v[32:39], v[136:139], v210, v211 op_sel_hi:[0,0,0]
	s_setprio 0
	s_setprio 1
	v_mfma_scale_f32_16x16x128_f8f6f4 v[188:191], v[8:15], v[56:63], v[188:191], v212, v211 op_sel_hi:[0,0,0]
	v_mfma_scale_f32_16x16x128_f8f6f4 v[180:183], v[0:7], v[56:63], v[180:183], v212, v211 op_sel_hi:[0,0,0]
	v_mfma_scale_f32_16x16x128_f8f6f4 v[172:175], v[8:15], v[48:55], v[172:175], v212, v211 op_sel_hi:[0,0,0]
	v_mfma_scale_f32_16x16x128_f8f6f4 v[164:167], v[0:7], v[48:55], v[164:167], v212, v211 op_sel_hi:[0,0,0]
	v_mfma_scale_f32_16x16x128_f8f6f4 v[156:159], v[8:15], v[40:47], v[156:159], v212, v211 op_sel_hi:[0,0,0]
	v_mfma_scale_f32_16x16x128_f8f6f4 v[148:151], v[0:7], v[40:47], v[148:151], v212, v211 op_sel_hi:[0,0,0]
	v_mfma_scale_f32_16x16x128_f8f6f4 v[140:143], v[8:15], v[32:39], v[140:143], v212, v211 op_sel_hi:[0,0,0]
	v_mfma_scale_f32_16x16x128_f8f6f4 v[132:135], v[0:7], v[32:39], v[132:135], v212, v211 op_sel_hi:[0,0,0]
	s_setprio 0
	s_barrier
	ds_read_b128 v[32:35], v209 offset:16384
	ds_read_b128 v[36:39], v209 offset:17408
	ds_read_b128 v[40:43], v209 offset:18432
	ds_read_b128 v[44:47], v209 offset:19456
	ds_read_b128 v[48:51], v209 offset:20480
	ds_read_b128 v[52:55], v209 offset:21504
	ds_read_b128 v[56:59], v209 offset:22528
	ds_read_b128 v[60:63], v209 offset:23552
	s_mov_b32 m0, s51
	s_nop 0
	global_load_lds_dwordx4 v200, s[42:43]
	s_mov_b32 m0, s53
	s_nop 0
	global_load_lds_dwordx4 v202, s[42:43]
	s_add_u32 s42, s42, s16
	s_addc_u32 s43, s43, s17
	s_mov_b32 m0, s55
	s_nop 0
	global_load_lds_dwordx4 v200, s[42:43]
	s_mov_b32 m0, s64
	s_nop 0
	global_load_lds_dwordx4 v202, s[42:43]
	s_mov_b32 m0, s47
	s_nop 0
	global_load_lds_dwordx4 v64, s[40:41]
	s_mov_b32 m0, s65
	s_nop 0
	global_load_lds_dwordx4 v65, s[40:41]
	s_waitcnt vmcnt(8)
	s_waitcnt lgkmcnt(0)
	s_barrier
	s_setprio 1
	s_waitcnt lgkmcnt(6)
	v_mfma_scale_f32_16x16x128_f8f6f4 v[128:131], v[24:31], v[32:39], v[128:131], v210, v211 op_sel_hi:[0,0,0]
	v_mfma_scale_f32_16x16x128_f8f6f4 v[120:123], v[16:23], v[32:39], v[120:123], v210, v211 op_sel_hi:[0,0,0]
	s_waitcnt lgkmcnt(4)
	v_mfma_scale_f32_16x16x128_f8f6f4 v[112:115], v[24:31], v[40:47], v[112:115], v210, v211 op_sel_hi:[0,0,0]
	v_mfma_scale_f32_16x16x128_f8f6f4 v[104:107], v[16:23], v[40:47], v[104:107], v210, v211 op_sel_hi:[0,0,0]
	s_waitcnt lgkmcnt(2)
	v_mfma_scale_f32_16x16x128_f8f6f4 v[96:99], v[24:31], v[48:55], v[96:99], v210, v211 op_sel_hi:[0,0,0]
	v_mfma_scale_f32_16x16x128_f8f6f4 v[88:91], v[16:23], v[48:55], v[88:91], v210, v211 op_sel_hi:[0,0,0]
	s_waitcnt lgkmcnt(0)
	v_mfma_scale_f32_16x16x128_f8f6f4 v[80:83], v[24:31], v[56:63], v[80:83], v210, v211 op_sel_hi:[0,0,0]
	v_mfma_scale_f32_16x16x128_f8f6f4 v[72:75], v[16:23], v[56:63], v[72:75], v210, v211 op_sel_hi:[0,0,0]
	s_setprio 0
	s_setprio 1
	v_mfma_scale_f32_16x16x128_f8f6f4 v[124:127], v[8:15], v[32:39], v[124:127], v212, v211 op_sel_hi:[0,0,0]
	v_mfma_scale_f32_16x16x128_f8f6f4 v[116:119], v[0:7], v[32:39], v[116:119], v212, v211 op_sel_hi:[0,0,0]
	v_mfma_scale_f32_16x16x128_f8f6f4 v[108:111], v[8:15], v[40:47], v[108:111], v212, v211 op_sel_hi:[0,0,0]
	v_mfma_scale_f32_16x16x128_f8f6f4 v[100:103], v[0:7], v[40:47], v[100:103], v212, v211 op_sel_hi:[0,0,0]
	v_mfma_scale_f32_16x16x128_f8f6f4 v[92:95], v[8:15], v[48:55], v[92:95], v212, v211 op_sel_hi:[0,0,0]
	v_mfma_scale_f32_16x16x128_f8f6f4 v[84:87], v[0:7], v[48:55], v[84:87], v212, v211 op_sel_hi:[0,0,0]
	v_mfma_scale_f32_16x16x128_f8f6f4 v[76:79], v[8:15], v[56:63], v[76:79], v212, v211 op_sel_hi:[0,0,0]
	v_mfma_scale_f32_16x16x128_f8f6f4 v[68:71], v[0:7], v[56:63], v[68:71], v212, v211 op_sel_hi:[0,0,0]
	s_setprio 0
	s_barrier
; #define PG8_STAGE(bufoff, gbase, voff) do { _Pragma("unroll") for (int _i = 0; _i < 2; ++_i) { unsigned keep_; \
;         asm volatile("s_mov_b32 %0, m0\n\ts_mov_b32 m0, %3\n\ts_nop 0\n\tglobal_load_lds_dwordx4 %1, %2\n\ts_mov_b32 m0, %0" : "=&s"(keep_) : "v"((voff)[_i]), "s"((const char*)(gbase)), "s"(ldsb + (unsigned)((bufoff) + _i * 8192)) : "memory"); } } while (0)
; #define PG8_LDA(dst, b, h) do { _Pragma("unroll") for (int m = 0; m < 4; ++m) _Pragma("unroll") for (int k = 0; k < 2; ++k) dst[m][k] = *(const PG8_LAS bf16x8*)(lds + PG8_SA(b, h) + aoff + m * 2048 + k * 1024); } while (0)
; #define PG8_LDB(dst, b, h) do { _Pragma("unroll") for (int n = 0; n < 2; ++n) _Pragma("unroll") for (int k = 0; k < 2; ++k) dst[n][k] = *(const PG8_LAS bf16x8*)(lds + PG8_SB(b, h) + boff + n * 2048 + k * 1024); } while (0)
; #define PG8_WAIT_V(n) asm volatile("s_waitcnt vmcnt(" #n ")" ::: "memory")
; #define PG8_WAIT_L(n) asm volatile("s_waitcnt lgkmcnt(" #n ")" ::: "memory")
; #define PG8_BAR __builtin_amdgcn_s_barrier()
; #define PG8_SCHED __builtin_amdgcn_sched_barrier(0)
; template <class Epi, class Sched, bool ALIGN_EPI, bool FP8 = false>
; __device__ __forceinline__ void gemm_phase(PG8_LAS unsigned char* lds, const Gemm g, const Sched& S, const Epi& E, const int wid, const int lane) {
;     ...
;             PG8_LDB(B0, 1, 0); PG8_LDB(B1, 1, 1); PG8_SCHED; PG8_LDA(At, 1, 0); PG8_STAGE(PG8_SA(0, 1), a2 + hstepA, vc1);
;             PG8_WAIT_V(8); PG8_WAIT_L(0); PG8_BAR; PG8_MMA(0, 0, At, B0); PG8_MMA(0, 1, At, B1); PG8_BAR; PG8_SCHED;
;             PG8_LDA(At, 1, 1); PG8_STAGE(PG8_SB(1, 0), b3, voffB); PG8_STAGE(PG8_SB(1, 1), b3 + hstep, voffB); PG8_STAGE(PG8_SA(1, 0), a3, vc0);
;             PG8_WAIT_V(8); PG8_WAIT_L(0); PG8_BAR; PG8_MMA(1, 0, At, B0); PG8_MMA(1, 1, At, B1); PG8_BAR; PG8_SCHED;
	v_add_u32_e32 v12, 0x18000, v206
	v_add_u32_e32 v28, 0x1c000, v206
	ds_read_b128 v[0:3], v12
	ds_read_b128 v[4:7], v12 offset:1024
	ds_read_b128 v[8:11], v12 offset:2048
	ds_read_b128 v[12:15], v12 offset:3072
	ds_read_b128 v[16:19], v28
	ds_read_b128 v[20:23], v28 offset:1024
	ds_read_b128 v[24:27], v28 offset:2048
	ds_read_b128 v[28:31], v28 offset:3072
	ds_read_b128 v[32:35], v209 offset:32768
	ds_read_b128 v[36:39], v209 offset:33792
	ds_read_b128 v[40:43], v209 offset:34816
	ds_read_b128 v[44:47], v209 offset:35840
	ds_read_b128 v[48:51], v209 offset:36864
	ds_read_b128 v[52:55], v209 offset:37888
	ds_read_b128 v[56:59], v209 offset:38912
	ds_read_b128 v[60:63], v209 offset:39936
	s_mov_b32 m0, s66
	s_nop 0
	global_load_lds_dwordx4 v66, s[40:41]
	s_mov_b32 m0, s67
	s_nop 0
	global_load_lds_dwordx4 v67, s[40:41]
	s_waitcnt vmcnt(8)
	s_waitcnt lgkmcnt(0)
	s_barrier
	s_setprio 1
	s_waitcnt lgkmcnt(6)
	v_mfma_scale_f32_16x16x128_f8f6f4 v[192:195], v[0:7], v[32:39], v[192:195], v210, v211 op_sel_hi:[0,0,0]
	v_mfma_scale_f32_16x16x128_f8f6f4 v[184:187], v[8:15], v[32:39], v[184:187], v210, v211 op_sel_hi:[0,0,0]
	s_waitcnt lgkmcnt(4)
	v_mfma_scale_f32_16x16x128_f8f6f4 v[176:179], v[0:7], v[40:47], v[176:179], v210, v211 op_sel_hi:[0,0,0]
	v_mfma_scale_f32_16x16x128_f8f6f4 v[168:171], v[8:15], v[40:47], v[168:171], v210, v211 op_sel_hi:[0,0,0]
	s_waitcnt lgkmcnt(2)
	v_mfma_scale_f32_16x16x128_f8f6f4 v[160:163], v[0:7], v[48:55], v[160:163], v210, v211 op_sel_hi:[0,0,0]
	v_mfma_scale_f32_16x16x128_f8f6f4 v[152:155], v[8:15], v[48:55], v[152:155], v210, v211 op_sel_hi:[0,0,0]
	s_waitcnt lgkmcnt(0)
	v_mfma_scale_f32_16x16x128_f8f6f4 v[144:147], v[0:7], v[56:63], v[144:147], v210, v211 op_sel_hi:[0,0,0]
	v_mfma_scale_f32_16x16x128_f8f6f4 v[136:139], v[8:15], v[56:63], v[136:139], v210, v211 op_sel_hi:[0,0,0]
	s_setprio 0
	s_setprio 1
	v_mfma_scale_f32_16x16x128_f8f6f4 v[188:191], v[16:23], v[32:39], v[188:191], v212, v211 op_sel_hi:[0,0,0]
	v_mfma_scale_f32_16x16x128_f8f6f4 v[180:183], v[24:31], v[32:39], v[180:183], v212, v211 op_sel_hi:[0,0,0]
	v_mfma_scale_f32_16x16x128_f8f6f4 v[172:175], v[16:23], v[40:47], v[172:175], v212, v211 op_sel_hi:[0,0,0]
	v_mfma_scale_f32_16x16x128_f8f6f4 v[164:167], v[24:31], v[40:47], v[164:167], v212, v211 op_sel_hi:[0,0,0]
	v_mfma_scale_f32_16x16x128_f8f6f4 v[156:159], v[16:23], v[48:55], v[156:159], v212, v211 op_sel_hi:[0,0,0]
	v_mfma_scale_f32_16x16x128_f8f6f4 v[148:151], v[24:31], v[48:55], v[148:151], v212, v211 op_sel_hi:[0,0,0]
	v_mfma_scale_f32_16x16x128_f8f6f4 v[140:143], v[16:23], v[56:63], v[140:143], v212, v211 op_sel_hi:[0,0,0]
	v_mfma_scale_f32_16x16x128_f8f6f4 v[132:135], v[24:31], v[56:63], v[132:135], v212, v211 op_sel_hi:[0,0,0]
	s_setprio 0
	s_barrier
	ds_read_b128 v[32:35], v209 offset:49152
	ds_read_b128 v[36:39], v209 offset:50176
	ds_read_b128 v[40:43], v209 offset:51200
	ds_read_b128 v[44:47], v209 offset:52224
	ds_read_b128 v[48:51], v209 offset:53248
	ds_read_b128 v[52:55], v209 offset:54272
	ds_read_b128 v[56:59], v209 offset:55296
	ds_read_b128 v[60:63], v209 offset:56320
	s_mov_b32 m0, s69
	s_nop 0
	global_load_lds_dwordx4 v200, s[38:39]
	s_mov_b32 m0, s70
	s_nop 0
	global_load_lds_dwordx4 v202, s[38:39]
	s_add_u32 s38, s38, s16
	s_addc_u32 s39, s39, s17
	s_mov_b32 m0, s73
	s_nop 0
	global_load_lds_dwordx4 v200, s[38:39]
	s_mov_b32 m0, s74
	s_nop 0
	global_load_lds_dwordx4 v202, s[38:39]
	s_mov_b32 m0, s71
	s_nop 0
	global_load_lds_dwordx4 v64, s[8:9]
	s_mov_b32 m0, s72
	s_nop 0
	global_load_lds_dwordx4 v65, s[8:9]
	s_waitcnt vmcnt(8)
	s_waitcnt lgkmcnt(0)
	s_barrier
	s_setprio 1
	s_waitcnt lgkmcnt(6)
	v_mfma_scale_f32_16x16x128_f8f6f4 v[128:131], v[0:7], v[32:39], v[128:131], v210, v211 op_sel_hi:[0,0,0]
	v_mfma_scale_f32_16x16x128_f8f6f4 v[120:123], v[8:15], v[32:39], v[120:123], v210, v211 op_sel_hi:[0,0,0]
	s_waitcnt lgkmcnt(4)
	v_mfma_scale_f32_16x16x128_f8f6f4 v[112:115], v[0:7], v[40:47], v[112:115], v210, v211 op_sel_hi:[0,0,0]
	v_mfma_scale_f32_16x16x128_f8f6f4 v[104:107], v[8:15], v[40:47], v[104:107], v210, v211 op_sel_hi:[0,0,0]
	s_waitcnt lgkmcnt(2)
	v_mfma_scale_f32_16x16x128_f8f6f4 v[96:99], v[0:7], v[48:55], v[96:99], v210, v211 op_sel_hi:[0,0,0]
	v_mfma_scale_f32_16x16x128_f8f6f4 v[88:91], v[8:15], v[48:55], v[88:91], v210, v211 op_sel_hi:[0,0,0]
	s_waitcnt lgkmcnt(0)
	v_mfma_scale_f32_16x16x128_f8f6f4 v[80:83], v[0:7], v[56:63], v[80:83], v210, v211 op_sel_hi:[0,0,0]
	v_mfma_scale_f32_16x16x128_f8f6f4 v[72:75], v[8:15], v[56:63], v[72:75], v210, v211 op_sel_hi:[0,0,0]
	s_setprio 0
	s_setprio 1
	v_mfma_scale_f32_16x16x128_f8f6f4 v[124:127], v[16:23], v[32:39], v[124:127], v212, v211 op_sel_hi:[0,0,0]
	v_mfma_scale_f32_16x16x128_f8f6f4 v[116:119], v[24:31], v[32:39], v[116:119], v212, v211 op_sel_hi:[0,0,0]
	v_mfma_scale_f32_16x16x128_f8f6f4 v[108:111], v[16:23], v[40:47], v[108:111], v212, v211 op_sel_hi:[0,0,0]
	v_mfma_scale_f32_16x16x128_f8f6f4 v[100:103], v[24:31], v[40:47], v[100:103], v212, v211 op_sel_hi:[0,0,0]
	v_mfma_scale_f32_16x16x128_f8f6f4 v[92:95], v[16:23], v[48:55], v[92:95], v212, v211 op_sel_hi:[0,0,0]
	v_mfma_scale_f32_16x16x128_f8f6f4 v[84:87], v[24:31], v[48:55], v[84:87], v212, v211 op_sel_hi:[0,0,0]
	v_mfma_scale_f32_16x16x128_f8f6f4 v[76:79], v[16:23], v[56:63], v[76:79], v212, v211 op_sel_hi:[0,0,0]
	v_mfma_scale_f32_16x16x128_f8f6f4 v[68:71], v[24:31], v[56:63], v[68:71], v212, v211 op_sel_hi:[0,0,0]
	s_setprio 0
	s_barrier
	s_add_u32 s6, s6, 0x100
	s_addc_u32 s7, s7, 0
	s_cmp_ge_i32 s89, s68
	s_cbranch_scc1 .LBB0_1659

; __device__ __forceinline__ unsigned pk4_fp8(float a, float b, float c, float d) { int r = __builtin_amdgcn_cvt_pk_fp8_f32(a, b, 0, false); r = __builtin_amdgcn_cvt_pk_fp8_f32(c, d, r, true); return (unsigned)r; }
;     __device__ __forceinline__ void operator()(const f32x4 (&acc)[2][2][4][2], const Unit& u, int wr, int wc, int fr, int fq) const {
;         const int row0 = u.pm * BM + wr * 64 + fr, col0 = (u.pn & 3) * 128 + wc * 32 + 8 * fq;
; #pragma unroll
;         for (int ai = 0; ai < 2; ++ai)
; #pragma unroll
;             for (int m = 0; m < 4; ++m) { float r[8];
; #pragma unroll
;                 for (int n = 0; n < 2; ++n)
; #pragma unroll
;                     for (int e = 0; e < 4; ++e) { const float g = acc[ai][0][m][n][e], up = acc[ai][1][m][n][e]; r[4 * n + e] = g * __builtin_amdgcn_rcpf(1.0f + __builtin_amdgcn_exp2f(-g * LOG2E)) * up * (float)(1 << ASHIFT); }
;                 v2u w; w.x = pk4_fp8(r[0], r[1], r[2], r[3]); w.y = pk4_fp8(r[4], r[5], r[6], r[7]);
;                 *(v2u*)(O + (size_t)(row0 + ai * HALF + m * 16) * EH + col0) = w; }
;     }
.LBB0_1661:
	s_mov_b32 s98, 0xbfb8aa3b
	s_nop 15
	s_nop 15
	v_lshl_add_u32 v4, s87, 8, v203
	s_lshl_b32 s6, s88, 7
	s_and_b32 s6, s6, 0x180
	v_ashrrev_i32_e32 v5, 31, v4
	v_add_u32_e32 v2, s6, v205
	v_lshlrev_b64 v[0:1], 9, v[4:5]
	v_ashrrev_i32_e32 v3, 31, v2
	v_lshl_add_u64 v[0:1], s[24:25], 0, v[0:1]
	v_lshl_add_u64 v[0:1], v[0:1], 0, v[2:3]
	v_pk_mul_f32 v[228:229], v[192:193], s[98:99] op_sel_hi:[1,0]
	v_pk_mul_f32 v[230:231], v[194:195], s[98:99] op_sel_hi:[1,0]
	v_pk_mul_f32 v[232:233], v[184:185], s[98:99] op_sel_hi:[1,0]
	v_pk_mul_f32 v[234:235], v[186:187], s[98:99] op_sel_hi:[1,0]
	v_exp_f32_e32 v228, v228
	v_exp_f32_e32 v229, v229
	v_exp_f32_e32 v230, v230
	v_exp_f32_e32 v231, v231
	v_exp_f32_e32 v232, v232
	v_exp_f32_e32 v233, v233
	v_exp_f32_e32 v234, v234
	v_exp_f32_e32 v235, v235
	v_pk_add_f32 v[228:229], v[228:229], 1.0 op_sel_hi:[1,0]
	v_pk_add_f32 v[230:231], v[230:231], 1.0 op_sel_hi:[1,0]
	v_pk_add_f32 v[232:233], v[232:233], 1.0 op_sel_hi:[1,0]
	v_pk_add_f32 v[234:235], v[234:235], 1.0 op_sel_hi:[1,0]
	v_rcp_f32_e32 v228, v228
	v_rcp_f32_e32 v229, v229
	v_rcp_f32_e32 v230, v230
	v_rcp_f32_e32 v231, v231
	v_rcp_f32_e32 v232, v232
	v_rcp_f32_e32 v233, v233
	v_rcp_f32_e32 v234, v234
	v_rcp_f32_e32 v235, v235
	v_pk_mul_f32 v[228:229], v[192:193], v[228:229]
	v_pk_mul_f32 v[230:231], v[194:195], v[230:231]
	v_pk_mul_f32 v[232:233], v[184:185], v[232:233]
	v_pk_mul_f32 v[234:235], v[186:187], v[234:235]
	v_pk_mul_f32 v[228:229], v[188:189], v[228:229]
	v_pk_mul_f32 v[230:231], v[190:191], v[230:231]
	v_pk_mul_f32 v[232:233], v[180:181], v[232:233]
	v_pk_mul_f32 v[234:235], v[182:183], v[234:235]
	v_mov_b32_e32 v244, 0
	v_mov_b32_e32 v245, 0
	v_cvt_pk_fp8_f32 v244, v228, v229
	v_cvt_pk_fp8_f32 v245, v232, v233
	v_cvt_pk_fp8_f32 v244, v230, v231 op_sel:[0,0,1]
	v_cvt_pk_fp8_f32 v245, v234, v235 op_sel:[0,0,1]
	s_nop 0
	global_store_dwordx2 v[0:1], v[244:245], off
	v_or_b32_e32 v8, 16, v4
	v_ashrrev_i32_e32 v9, 31, v8
	v_lshlrev_b64 v[8:9], 9, v[8:9]
	v_lshl_add_u64 v[8:9], s[24:25], 0, v[8:9]
	v_lshl_add_u64 v[8:9], v[8:9], 0, v[2:3]
	v_pk_mul_f32 v[228:229], v[176:177], s[98:99] op_sel_hi:[1,0]
	v_pk_mul_f32 v[230:231], v[178:179], s[98:99] op_sel_hi:[1,0]
	v_pk_mul_f32 v[232:233], v[168:169], s[98:99] op_sel_hi:[1,0]
	v_pk_mul_f32 v[234:235], v[170:171], s[98:99] op_sel_hi:[1,0]
	v_exp_f32_e32 v228, v228
	v_exp_f32_e32 v229, v229
	v_exp_f32_e32 v230, v230
	v_exp_f32_e32 v231, v231
	v_exp_f32_e32 v232, v232
	v_exp_f32_e32 v233, v233
	v_exp_f32_e32 v234, v234
	v_exp_f32_e32 v235, v235
	v_pk_add_f32 v[228:229], v[228:229], 1.0 op_sel_hi:[1,0]
	v_pk_add_f32 v[230:231], v[230:231], 1.0 op_sel_hi:[1,0]
	v_pk_add_f32 v[232:233], v[232:233], 1.0 op_sel_hi:[1,0]
	v_pk_add_f32 v[234:235], v[234:235], 1.0 op_sel_hi:[1,0]
	v_rcp_f32_e32 v228, v228
	v_rcp_f32_e32 v229, v229
	v_rcp_f32_e32 v230, v230
	v_rcp_f32_e32 v231, v231
	v_rcp_f32_e32 v232, v232
	v_rcp_f32_e32 v233, v233
	v_rcp_f32_e32 v234, v234
	v_rcp_f32_e32 v235, v235
	v_pk_mul_f32 v[228:229], v[176:177], v[228:229]
	v_pk_mul_f32 v[230:231], v[178:179], v[230:231]
	v_pk_mul_f32 v[232:233], v[168:169], v[232:233]
	v_pk_mul_f32 v[234:235], v[170:171], v[234:235]
	v_pk_mul_f32 v[228:229], v[172:173], v[228:229]
	v_pk_mul_f32 v[230:231], v[174:175], v[230:231]
	v_pk_mul_f32 v[232:233], v[164:165], v[232:233]
	v_pk_mul_f32 v[234:235], v[166:167], v[234:235]
	v_mov_b32_e32 v244, 0
	v_mov_b32_e32 v245, 0
	v_cvt_pk_fp8_f32 v244, v228, v229
	v_cvt_pk_fp8_f32 v245, v232, v233
	v_cvt_pk_fp8_f32 v244, v230, v231 op_sel:[0,0,1]
	v_cvt_pk_fp8_f32 v245, v234, v235 op_sel:[0,0,1]
	s_nop 0
	global_store_dwordx2 v[8:9], v[244:245], off
	v_or_b32_e32 v8, 32, v4
	v_ashrrev_i32_e32 v9, 31, v8
	v_lshlrev_b64 v[8:9], 9, v[8:9]
	v_lshl_add_u64 v[8:9], s[24:25], 0, v[8:9]
	v_lshl_add_u64 v[8:9], v[8:9], 0, v[2:3]
	v_pk_mul_f32 v[228:229], v[160:161], s[98:99] op_sel_hi:[1,0]
	v_pk_mul_f32 v[230:231], v[162:163], s[98:99] op_sel_hi:[1,0]
	v_pk_mul_f32 v[232:233], v[152:153], s[98:99] op_sel_hi:[1,0]
	v_pk_mul_f32 v[234:235], v[154:155], s[98:99] op_sel_hi:[1,0]
	v_exp_f32_e32 v228, v228
	v_exp_f32_e32 v229, v229
	v_exp_f32_e32 v230, v230
	v_exp_f32_e32 v231, v231
	v_exp_f32_e32 v232, v232
	v_exp_f32_e32 v233, v233
	v_exp_f32_e32 v234, v234
	v_exp_f32_e32 v235, v235
	v_pk_add_f32 v[228:229], v[228:229], 1.0 op_sel_hi:[1,0]
	v_pk_add_f32 v[230:231], v[230:231], 1.0 op_sel_hi:[1,0]
	v_pk_add_f32 v[232:233], v[232:233], 1.0 op_sel_hi:[1,0]
	v_pk_add_f32 v[234:235], v[234:235], 1.0 op_sel_hi:[1,0]
	v_rcp_f32_e32 v228, v228
	v_rcp_f32_e32 v229, v229
	v_rcp_f32_e32 v230, v230
	v_rcp_f32_e32 v231, v231
	v_rcp_f32_e32 v232, v232
	v_rcp_f32_e32 v233, v233
	v_rcp_f32_e32 v234, v234
	v_rcp_f32_e32 v235, v235
	v_pk_mul_f32 v[228:229], v[160:161], v[228:229]
	v_pk_mul_f32 v[230:231], v[162:163], v[230:231]
	v_pk_mul_f32 v[232:233], v[152:153], v[232:233]
	v_pk_mul_f32 v[234:235], v[154:155], v[234:235]
	v_pk_mul_f32 v[228:229], v[156:157], v[228:229]
	v_pk_mul_f32 v[230:231], v[158:159], v[230:231]
	v_pk_mul_f32 v[232:233], v[148:149], v[232:233]
	v_pk_mul_f32 v[234:235], v[150:151], v[234:235]
	v_mov_b32_e32 v244, 0
	v_mov_b32_e32 v245, 0
	v_cvt_pk_fp8_f32 v244, v228, v229
	v_cvt_pk_fp8_f32 v245, v232, v233
	v_cvt_pk_fp8_f32 v244, v230, v231 op_sel:[0,0,1]
	v_cvt_pk_fp8_f32 v245, v234, v235 op_sel:[0,0,1]
	s_nop 0
	global_store_dwordx2 v[8:9], v[244:245], off
	v_or_b32_e32 v4, 48, v4
	v_ashrrev_i32_e32 v5, 31, v4
	v_lshlrev_b64 v[4:5], 9, v[4:5]
	v_lshl_add_u64 v[4:5], s[24:25], 0, v[4:5]
	v_lshl_add_u64 v[2:3], v[4:5], 0, v[2:3]
	v_pk_mul_f32 v[228:229], v[144:145], s[98:99] op_sel_hi:[1,0]
; __device__ __forceinline__ unsigned pk4_fp8(float a, float b, float c, float d) { int r = __builtin_amdgcn_cvt_pk_fp8_f32(a, b, 0, false); r = __builtin_amdgcn_cvt_pk_fp8_f32(c, d, r, true); return (unsigned)r; }
;     __device__ __forceinline__ void operator()(const f32x4 (&acc)[2][2][4][2], const Unit& u, int wr, int wc, int fr, int fq) const {
;         const int row0 = u.pm * BM + wr * 64 + fr, col0 = (u.pn & 3) * 128 + wc * 32 + 8 * fq;
; #pragma unroll
;         for (int ai = 0; ai < 2; ++ai)
; #pragma unroll
;             for (int m = 0; m < 4; ++m) { float r[8];
; #pragma unroll
;                 for (int n = 0; n < 2; ++n)
; #pragma unroll
;                     for (int e = 0; e < 4; ++e) { const float g = acc[ai][0][m][n][e], up = acc[ai][1][m][n][e]; r[4 * n + e] = g * __builtin_amdgcn_rcpf(1.0f + __builtin_amdgcn_exp2f(-g * LOG2E)) * up * (float)(1 << ASHIFT); }
;                 v2u w; w.x = pk4_fp8(r[0], r[1], r[2], r[3]); w.y = pk4_fp8(r[4], r[5], r[6], r[7]);
;                 *(v2u*)(O + (size_t)(row0 + ai * HALF + m * 16) * EH + col0) = w; }
;     }
	v_pk_mul_f32 v[230:231], v[146:147], s[98:99] op_sel_hi:[1,0]
	v_pk_mul_f32 v[232:233], v[136:137], s[98:99] op_sel_hi:[1,0]
	v_pk_mul_f32 v[234:235], v[138:139], s[98:99] op_sel_hi:[1,0]
	v_exp_f32_e32 v228, v228
	v_exp_f32_e32 v229, v229
	v_exp_f32_e32 v230, v230
	v_exp_f32_e32 v231, v231
	v_exp_f32_e32 v232, v232
	v_exp_f32_e32 v233, v233
	v_exp_f32_e32 v234, v234
	v_exp_f32_e32 v235, v235
	v_pk_add_f32 v[228:229], v[228:229], 1.0 op_sel_hi:[1,0]
	v_pk_add_f32 v[230:231], v[230:231], 1.0 op_sel_hi:[1,0]
	v_pk_add_f32 v[232:233], v[232:233], 1.0 op_sel_hi:[1,0]
	v_pk_add_f32 v[234:235], v[234:235], 1.0 op_sel_hi:[1,0]
	v_rcp_f32_e32 v228, v228
	v_rcp_f32_e32 v229, v229
	v_rcp_f32_e32 v230, v230
	v_rcp_f32_e32 v231, v231
	v_rcp_f32_e32 v232, v232
	v_rcp_f32_e32 v233, v233
	v_rcp_f32_e32 v234, v234
	v_rcp_f32_e32 v235, v235
	v_pk_mul_f32 v[228:229], v[144:145], v[228:229]
	v_pk_mul_f32 v[230:231], v[146:147], v[230:231]
	v_pk_mul_f32 v[232:233], v[136:137], v[232:233]
	v_pk_mul_f32 v[234:235], v[138:139], v[234:235]
	v_pk_mul_f32 v[228:229], v[140:141], v[228:229]
	v_pk_mul_f32 v[230:231], v[142:143], v[230:231]
	v_pk_mul_f32 v[232:233], v[132:133], v[232:233]
	v_pk_mul_f32 v[234:235], v[134:135], v[234:235]
	v_mov_b32_e32 v244, 0
	v_mov_b32_e32 v245, 0
	v_cvt_pk_fp8_f32 v244, v228, v229
	v_cvt_pk_fp8_f32 v245, v232, v233
	v_cvt_pk_fp8_f32 v244, v230, v231 op_sel:[0,0,1]
	v_cvt_pk_fp8_f32 v245, v234, v235 op_sel:[0,0,1]
	s_nop 0
	global_store_dwordx2 v[2:3], v[244:245], off
	v_add_co_u32_e32 v4, vcc, s50, v0
	s_nop 0
	v_addc_co_u32_e32 v5, vcc, 0, v1, vcc
	v_pk_mul_f32 v[228:229], v[128:129], s[98:99] op_sel_hi:[1,0]
	v_pk_mul_f32 v[230:231], v[130:131], s[98:99] op_sel_hi:[1,0]
	v_pk_mul_f32 v[232:233], v[120:121], s[98:99] op_sel_hi:[1,0]
	v_pk_mul_f32 v[234:235], v[122:123], s[98:99] op_sel_hi:[1,0]
	v_exp_f32_e32 v228, v228
	v_exp_f32_e32 v229, v229
	v_exp_f32_e32 v230, v230
	v_exp_f32_e32 v231, v231
	v_exp_f32_e32 v232, v232
	v_exp_f32_e32 v233, v233
	v_exp_f32_e32 v234, v234
	v_exp_f32_e32 v235, v235
	v_pk_add_f32 v[228:229], v[228:229], 1.0 op_sel_hi:[1,0]
	v_pk_add_f32 v[230:231], v[230:231], 1.0 op_sel_hi:[1,0]
	v_pk_add_f32 v[232:233], v[232:233], 1.0 op_sel_hi:[1,0]
	v_pk_add_f32 v[234:235], v[234:235], 1.0 op_sel_hi:[1,0]
	v_rcp_f32_e32 v228, v228
	v_rcp_f32_e32 v229, v229
	v_rcp_f32_e32 v230, v230
	v_rcp_f32_e32 v231, v231
	v_rcp_f32_e32 v232, v232
	v_rcp_f32_e32 v233, v233
	v_rcp_f32_e32 v234, v234
	v_rcp_f32_e32 v235, v235
	v_pk_mul_f32 v[228:229], v[128:129], v[228:229]
	v_pk_mul_f32 v[230:231], v[130:131], v[230:231]
	v_pk_mul_f32 v[232:233], v[120:121], v[232:233]
	v_pk_mul_f32 v[234:235], v[122:123], v[234:235]
	v_pk_mul_f32 v[228:229], v[124:125], v[228:229]
	v_pk_mul_f32 v[230:231], v[126:127], v[230:231]
	v_pk_mul_f32 v[232:233], v[116:117], v[232:233]
	v_pk_mul_f32 v[234:235], v[118:119], v[234:235]
	v_mov_b32_e32 v244, 0
	v_mov_b32_e32 v245, 0
	v_cvt_pk_fp8_f32 v244, v228, v229
	v_cvt_pk_fp8_f32 v245, v232, v233
	v_cvt_pk_fp8_f32 v244, v230, v231 op_sel:[0,0,1]
	v_cvt_pk_fp8_f32 v245, v234, v235 op_sel:[0,0,1]
	s_nop 0
	global_store_dwordx2 v[4:5], v[244:245], off
	v_add_co_u32_e32 v4, vcc, s52, v0
	s_nop 0
	v_addc_co_u32_e32 v5, vcc, 0, v1, vcc
	v_pk_mul_f32 v[228:229], v[112:113], s[98:99] op_sel_hi:[1,0]
	v_pk_mul_f32 v[230:231], v[114:115], s[98:99] op_sel_hi:[1,0]
	v_pk_mul_f32 v[232:233], v[104:105], s[98:99] op_sel_hi:[1,0]
	v_pk_mul_f32 v[234:235], v[106:107], s[98:99] op_sel_hi:[1,0]
	v_exp_f32_e32 v228, v228
	v_exp_f32_e32 v229, v229
	v_exp_f32_e32 v230, v230
	v_exp_f32_e32 v231, v231
	v_exp_f32_e32 v232, v232
	v_exp_f32_e32 v233, v233
	v_exp_f32_e32 v234, v234
	v_exp_f32_e32 v235, v235
	v_pk_add_f32 v[228:229], v[228:229], 1.0 op_sel_hi:[1,0]
	v_pk_add_f32 v[230:231], v[230:231], 1.0 op_sel_hi:[1,0]
	v_pk_add_f32 v[232:233], v[232:233], 1.0 op_sel_hi:[1,0]
	v_pk_add_f32 v[234:235], v[234:235], 1.0 op_sel_hi:[1,0]
	v_rcp_f32_e32 v228, v228
	v_rcp_f32_e32 v229, v229
	v_rcp_f32_e32 v230, v230
	v_rcp_f32_e32 v231, v231
	v_rcp_f32_e32 v232, v232
	v_rcp_f32_e32 v233, v233
	v_rcp_f32_e32 v234, v234
; __device__ __forceinline__ unsigned pk4_fp8(float a, float b, float c, float d) { int r = __builtin_amdgcn_cvt_pk_fp8_f32(a, b, 0, false); r = __builtin_amdgcn_cvt_pk_fp8_f32(c, d, r, true); return (unsigned)r; }
;     __device__ __forceinline__ void operator()(const f32x4 (&acc)[2][2][4][2], const Unit& u, int wr, int wc, int fr, int fq) const {
;         const int row0 = u.pm * BM + wr * 64 + fr, col0 = (u.pn & 3) * 128 + wc * 32 + 8 * fq;
; #pragma unroll
;         for (int ai = 0; ai < 2; ++ai)
; #pragma unroll
;             for (int m = 0; m < 4; ++m) { float r[8];
; #pragma unroll
;                 for (int n = 0; n < 2; ++n)
; #pragma unroll
;                     for (int e = 0; e < 4; ++e) { const float g = acc[ai][0][m][n][e], up = acc[ai][1][m][n][e]; r[4 * n + e] = g * __builtin_amdgcn_rcpf(1.0f + __builtin_amdgcn_exp2f(-g * LOG2E)) * up * (float)(1 << ASHIFT); }
;                 v2u w; w.x = pk4_fp8(r[0], r[1], r[2], r[3]); w.y = pk4_fp8(r[4], r[5], r[6], r[7]);
;                 *(v2u*)(O + (size_t)(row0 + ai * HALF + m * 16) * EH + col0) = w; }
;     }
	v_rcp_f32_e32 v235, v235
	v_pk_mul_f32 v[228:229], v[112:113], v[228:229]
	v_pk_mul_f32 v[230:231], v[114:115], v[230:231]
	v_pk_mul_f32 v[232:233], v[104:105], v[232:233]
	v_pk_mul_f32 v[234:235], v[106:107], v[234:235]
	v_pk_mul_f32 v[228:229], v[108:109], v[228:229]
	v_pk_mul_f32 v[230:231], v[110:111], v[230:231]
	v_pk_mul_f32 v[232:233], v[100:101], v[232:233]
	v_pk_mul_f32 v[234:235], v[102:103], v[234:235]
	v_mov_b32_e32 v244, 0
	v_mov_b32_e32 v245, 0
	v_cvt_pk_fp8_f32 v244, v228, v229
	v_cvt_pk_fp8_f32 v245, v232, v233
	v_cvt_pk_fp8_f32 v244, v230, v231 op_sel:[0,0,1]
	v_cvt_pk_fp8_f32 v245, v234, v235 op_sel:[0,0,1]
	s_nop 0
	global_store_dwordx2 v[4:5], v[244:245], off
	v_add_co_u32_e32 v4, vcc, s54, v0
	s_nop 0
	v_addc_co_u32_e32 v5, vcc, 0, v1, vcc
	v_pk_mul_f32 v[228:229], v[96:97], s[98:99] op_sel_hi:[1,0]
	v_pk_mul_f32 v[230:231], v[98:99], s[98:99] op_sel_hi:[1,0]
	v_pk_mul_f32 v[232:233], v[88:89], s[98:99] op_sel_hi:[1,0]
	v_pk_mul_f32 v[234:235], v[90:91], s[98:99] op_sel_hi:[1,0]
	v_exp_f32_e32 v228, v228
	v_exp_f32_e32 v229, v229
	v_exp_f32_e32 v230, v230
	v_exp_f32_e32 v231, v231
	v_exp_f32_e32 v232, v232
	v_exp_f32_e32 v233, v233
	v_exp_f32_e32 v234, v234
	v_exp_f32_e32 v235, v235
	v_pk_add_f32 v[228:229], v[228:229], 1.0 op_sel_hi:[1,0]
	v_pk_add_f32 v[230:231], v[230:231], 1.0 op_sel_hi:[1,0]
	v_pk_add_f32 v[232:233], v[232:233], 1.0 op_sel_hi:[1,0]
	v_pk_add_f32 v[234:235], v[234:235], 1.0 op_sel_hi:[1,0]
	v_rcp_f32_e32 v228, v228
	v_rcp_f32_e32 v229, v229
	v_rcp_f32_e32 v230, v230
	v_rcp_f32_e32 v231, v231
	v_rcp_f32_e32 v232, v232
	v_rcp_f32_e32 v233, v233
	v_rcp_f32_e32 v234, v234
	v_rcp_f32_e32 v235, v235
	v_pk_mul_f32 v[228:229], v[96:97], v[228:229]
	v_pk_mul_f32 v[230:231], v[98:99], v[230:231]
	v_pk_mul_f32 v[232:233], v[88:89], v[232:233]
	v_pk_mul_f32 v[234:235], v[90:91], v[234:235]
	v_pk_mul_f32 v[228:229], v[92:93], v[228:229]
	v_pk_mul_f32 v[230:231], v[94:95], v[230:231]
	v_pk_mul_f32 v[232:233], v[84:85], v[232:233]
	v_pk_mul_f32 v[234:235], v[86:87], v[234:235]
	v_mov_b32_e32 v244, 0
	v_mov_b32_e32 v245, 0
	v_cvt_pk_fp8_f32 v244, v228, v229
	v_cvt_pk_fp8_f32 v245, v232, v233
	v_cvt_pk_fp8_f32 v244, v230, v231 op_sel:[0,0,1]
	v_cvt_pk_fp8_f32 v245, v234, v235 op_sel:[0,0,1]
	s_nop 0
	global_store_dwordx2 v[4:5], v[244:245], off
	v_add_co_u32_e32 v0, vcc, 0x16000, v0
	s_nop 1
	v_addc_co_u32_e32 v1, vcc, 0, v1, vcc
	s_and_b64 vcc, exec, s[4:5]
	s_mov_b64 s[4:5], -1
	v_pk_mul_f32 v[228:229], v[80:81], s[98:99] op_sel_hi:[1,0]
	v_pk_mul_f32 v[230:231], v[82:83], s[98:99] op_sel_hi:[1,0]
	v_pk_mul_f32 v[232:233], v[72:73], s[98:99] op_sel_hi:[1,0]
	v_pk_mul_f32 v[234:235], v[74:75], s[98:99] op_sel_hi:[1,0]
	v_exp_f32_e32 v228, v228
	v_exp_f32_e32 v229, v229
	v_exp_f32_e32 v230, v230
	v_exp_f32_e32 v231, v231
	v_exp_f32_e32 v232, v232
	v_exp_f32_e32 v233, v233
	v_exp_f32_e32 v234, v234
	v_exp_f32_e32 v235, v235
	v_pk_add_f32 v[228:229], v[228:229], 1.0 op_sel_hi:[1,0]
	v_pk_add_f32 v[230:231], v[230:231], 1.0 op_sel_hi:[1,0]
	v_pk_add_f32 v[232:233], v[232:233], 1.0 op_sel_hi:[1,0]
	v_pk_add_f32 v[234:235], v[234:235], 1.0 op_sel_hi:[1,0]
	v_rcp_f32_e32 v228, v228
	v_rcp_f32_e32 v229, v229
	v_rcp_f32_e32 v230, v230
	v_rcp_f32_e32 v231, v231
	v_rcp_f32_e32 v232, v232
	v_rcp_f32_e32 v233, v233
	v_rcp_f32_e32 v234, v234
	v_rcp_f32_e32 v235, v235
	v_pk_mul_f32 v[228:229], v[80:81], v[228:229]
	v_pk_mul_f32 v[230:231], v[82:83], v[230:231]
	v_pk_mul_f32 v[232:233], v[72:73], v[232:233]
	v_pk_mul_f32 v[234:235], v[74:75], v[234:235]
	v_pk_mul_f32 v[228:229], v[76:77], v[228:229]
	v_pk_mul_f32 v[230:231], v[78:79], v[230:231]
	v_pk_mul_f32 v[232:233], v[68:69], v[232:233]
	v_pk_mul_f32 v[234:235], v[70:71], v[234:235]
	v_mov_b32_e32 v244, 0
	v_mov_b32_e32 v245, 0
	v_cvt_pk_fp8_f32 v244, v228, v229
	v_cvt_pk_fp8_f32 v245, v232, v233
	v_cvt_pk_fp8_f32 v244, v230, v231 op_sel:[0,0,1]
	v_cvt_pk_fp8_f32 v245, v234, v235 op_sel:[0,0,1]
	s_nop 0
	global_store_dwordx2 v[0:1], v[244:245], off
	s_cbranch_vccnz .LBB0_1625
	s_andn2_b64 vcc, exec, s[22:23]
	s_cbranch_vccnz .LBB0_1624
	s_barrier
	s_branch .LBB0_1624
